# pool: L2 prefetch of the next item's window rows issued in the column pass
# baseline (speedup 1.0000x reference)
; #define LAS __attribute__((address_space(3)))
; __device__ __forceinline__ unsigned pk2(float lo, float hi) { return f2bf(lo) | (f2bf(hi) << 16); }
; template <int HALFW>
; __device__ __forceinline__ void pool_item(const bf16* P, bf16* DP, LAS float* tmp, int tid, int b, int r, int g) {
;     const int rlo = r - HALFW < 0 ? 0 : r - HALFW, rhi = r + HALFW > 32 ? 32 : r + HALFW;
;     const float rinv = 1.f / (float)(rhi - rlo);
; #pragma unroll 1
;     for (int q = 0; q < 4; ++q) { const int p = tid + 512 * q, c = p >> 5, ch0 = (p & 31) * 8; float acc[8]; v4u x[2 * HALFW];
; #pragma unroll
;         for (int u = 0; u < 2 * HALFW; ++u) { const int rr = (rlo + u < rhi) ? rlo + u : rlo; x[u] = *(const v4u*)(P + ((size_t)(b * 2048 + rr * 64 + c)) * 1024 + g * 256 + ch0); }
;     ...
;         *(LAS f32x4*)(tmp + c * 256 + ch0) = (f32x4){acc[0] * rinv, acc[1] * rinv, acc[2] * rinv, acc[3] * rinv};
;         *(LAS f32x4*)(tmp + c * 256 + ch0 + 4) = (f32x4){acc[4] * rinv, acc[5] * rinv, acc[6] * rinv, acc[7] * rinv}; }
;     __syncthreads();
; #pragma unroll 1
;     for (int q = 0; q < 4; ++q) { const int p = tid + 512 * q, c = p >> 5, ch0 = (p & 31) * 8;
;         const int clo = c - HALFW < 0 ? 0 : c - HALFW, chi = c + HALFW > 64 ? 64 : c + HALFW; const float cinv = 1.f / (float)(chi - clo);
;         const size_t o = ((size_t)(b * 2048 + r * 64 + c)) * 1024 + g * 256 + ch0;
;         const v4u x = *(const v4u*)(P + o);
;         f32x4 a0 = (f32x4){0.f, 0.f, 0.f, 0.f}, a1 = a0;
; #pragma unroll
;         for (int u = 0; u < 2 * HALFW; ++u) { const int cc = (clo + u < chi) ? clo + u : clo; const float m = (clo + u < chi) ? 1.f : 0.f;
;             a0 += *(const LAS f32x4*)(tmp + cc * 256 + ch0) * m; a1 += *(const LAS f32x4*)(tmp + cc * 256 + ch0 + 4) * m; }
;         v4u d; d.x = pk2(a0[0] * cinv - bflo(x.x), a0[1] * cinv - bfhi(x.x)); d.y = pk2(a0[2] * cinv - bflo(x.y), a0[3] * cinv - bfhi(x.y));
;         d.z = pk2(a1[0] * cinv - bflo(x.z), a1[1] * cinv - bfhi(x.z)); d.w = pk2(a1[2] * cinv - bflo(x.w), a1[3] * cinv - bfhi(x.w));
;         *(v4u*)(DP + o) = d; }
.Lpool_h2_q3:
	v_pk_mul_f32 v[52:53], v[52:53], v[48:49] op_sel_hi:[1,0]
	v_pk_mul_f32 v[54:55], v[54:55], v[48:49] op_sel_hi:[1,0]
	v_pk_mul_f32 v[56:57], v[56:57], v[48:49] op_sel_hi:[1,0]
	v_pk_mul_f32 v[58:59], v[58:59], v[48:49] op_sel_hi:[1,0]
	ds_write_b128 v49, v[52:55] offset:49152
	ds_write_b128 v49, v[56:59] offset:49168
	v_add_u32_e32 v51, 0, v50
	v_add_u32_e32 v60, 2, v51
	v_min_u32_e32 v60, 64, v60
	v_sub_u32_e64 v61, v51, 2 clamp
	v_sub_u32_e32 v60, v60, v61
	v_cvt_f32_u32_e32 v212, v60
	v_div_scale_f32 v213, s[30:31], v212, v212, 1.0
	v_div_scale_f32 v215, vcc, 1.0, v212, 1.0
	v_rcp_f32_e32 v214, v213
	s_nop 1
	v_fma_f32 v216, -v213, v214, 1.0
	v_fmac_f32_e32 v214, v216, v214
	v_mul_f32_e32 v216, v215, v214
	v_fma_f32 v217, -v213, v216, v215
	v_fmac_f32_e32 v216, v217, v214
	v_fma_f32 v213, -v213, v216, v215
	s_nop 1
	v_div_fmas_f32 v213, v213, v214, v216
	v_div_fixup_f32 v196, v213, v212, 1.0
	v_add_u32_e32 v51, 16, v50
	v_add_u32_e32 v60, 2, v51
	v_min_u32_e32 v60, 64, v60
	v_sub_u32_e64 v61, v51, 2 clamp
	v_sub_u32_e32 v60, v60, v61
	v_cvt_f32_u32_e32 v212, v60
	v_div_scale_f32 v213, s[30:31], v212, v212, 1.0
	v_div_scale_f32 v215, vcc, 1.0, v212, 1.0
	v_rcp_f32_e32 v214, v213
	s_nop 1
	v_fma_f32 v216, -v213, v214, 1.0
	v_fmac_f32_e32 v214, v216, v214
	v_mul_f32_e32 v216, v215, v214
	v_fma_f32 v217, -v213, v216, v215
	v_fmac_f32_e32 v216, v217, v214
	v_fma_f32 v213, -v213, v216, v215
	s_nop 1
	v_div_fmas_f32 v213, v213, v214, v216
	v_div_fixup_f32 v198, v213, v212, 1.0
	v_add_u32_e32 v51, 32, v50
	v_add_u32_e32 v60, 2, v51
	v_min_u32_e32 v60, 64, v60
	v_sub_u32_e64 v61, v51, 2 clamp
	v_sub_u32_e32 v60, v60, v61
	v_cvt_f32_u32_e32 v212, v60
	v_div_scale_f32 v213, s[30:31], v212, v212, 1.0
	v_div_scale_f32 v215, vcc, 1.0, v212, 1.0
	v_rcp_f32_e32 v214, v213
	s_nop 1
	v_fma_f32 v216, -v213, v214, 1.0
	v_fmac_f32_e32 v214, v216, v214
	v_mul_f32_e32 v216, v215, v214
	v_fma_f32 v217, -v213, v216, v215
	v_fmac_f32_e32 v216, v217, v214
	v_fma_f32 v213, -v213, v216, v215
	s_nop 1
	v_div_fmas_f32 v213, v213, v214, v216
	v_div_fixup_f32 v200, v213, v212, 1.0
	v_add_u32_e32 v51, 48, v50
	v_add_u32_e32 v60, 2, v51
	v_min_u32_e32 v60, 64, v60
	v_sub_u32_e64 v61, v51, 2 clamp
	v_sub_u32_e32 v60, v60, v61
	v_cvt_f32_u32_e32 v212, v60
	v_div_scale_f32 v213, s[30:31], v212, v212, 1.0
	v_div_scale_f32 v215, vcc, 1.0, v212, 1.0
	v_rcp_f32_e32 v214, v213
	s_nop 1
	v_fma_f32 v216, -v213, v214, 1.0
	v_fmac_f32_e32 v214, v216, v214
	v_mul_f32_e32 v216, v215, v214
	v_fma_f32 v217, -v213, v216, v215
	v_fmac_f32_e32 v216, v217, v214
	v_fma_f32 v213, -v213, v216, v215
	s_nop 1
	v_div_fmas_f32 v213, v213, v214, v216
	v_div_fixup_f32 v202, v213, v212, 1.0
	s_waitcnt lgkmcnt(0)
	s_barrier
	v_add_u32_e32 v51, -2, v50
	v_add_u32_e32 v60, 0, v51
	v_min_u32_e32 v60, 64, v60
	v_lshl_add_u32 v60, v60, 10, v3
	ds_read_b128 v[204:207], v60
	ds_read_b128 v[208:211], v60 offset:16
	v_add_u32_e32 v60, 1, v51
	v_min_u32_e32 v60, 64, v60
	v_lshl_add_u32 v60, v60, 10, v3
	ds_read_b128 v[76:79], v60
	ds_read_b128 v[80:83], v60 offset:16
	v_add_u32_e32 v60, 2, v51
	v_min_u32_e32 v60, 64, v60
	v_lshl_add_u32 v60, v60, 10, v3
	ds_read_b128 v[84:87], v60
	ds_read_b128 v[88:91], v60 offset:16
	v_add_u32_e32 v60, 3, v51
	v_min_u32_e32 v60, 64, v60
	v_lshl_add_u32 v60, v60, 10, v3
	ds_read_b128 v[92:95], v60
	ds_read_b128 v[96:99], v60 offset:16
	s_waitcnt lgkmcnt(4)
	v_pk_add_f32 v[204:205], v[204:205], v[76:77]
	v_pk_add_f32 v[206:207], v[206:207], v[78:79]
	v_pk_add_f32 v[208:209], v[208:209], v[80:81]
	v_pk_add_f32 v[210:211], v[210:211], v[82:83]
	s_waitcnt lgkmcnt(0)
	v_pk_add_f32 v[204:205], v[204:205], v[84:85]
	v_pk_add_f32 v[206:207], v[206:207], v[86:87]
	v_pk_add_f32 v[208:209], v[208:209], v[88:89]
	v_pk_add_f32 v[210:211], v[210:211], v[90:91]
	v_pk_add_f32 v[204:205], v[204:205], v[92:93]
	v_pk_add_f32 v[206:207], v[206:207], v[94:95]
	v_pk_add_f32 v[208:209], v[208:209], v[96:97]
	v_pk_add_f32 v[210:211], v[210:211], v[98:99]
	s_waitcnt vmcnt(0)
	s_sub_i32 s39, s37, 1
	s_max_i32 s39, s39, 0
	s_add_i32 s40, s37, 1
	s_min_i32 s40, s40, 32
	s_sub_i32 s41, s40, s39
	s_add_i32 s41, s41, -1
	s_lshl_b32 s39, s39, 6
	s_add_i32 s39, s29, s39
	s_lshl_b32 s39, s39, 11
	s_add_u32 s50, s44, s39
	s_addc_u32 s51, s45, 0
	v_lshrrev_b32_e32 v240, 8, v66
	v_bfe_u32 v241, v66, 2, 6
	v_and_b32_e32 v242, 3, v66
	v_lshlrev_b32_e32 v241, 11, v241
	v_lshl_or_b32 v241, v242, 7, v241
	v_min_u32_e32 v242, s41, v240
	v_lshl_add_u32 v243, v242, 17, v241
	global_load_dword v244, v243, s[50:51]
	v_lshlrev_b32_e32 v40, 16, v16
	v_and_b32_e32 v41, 0xffff0000, v16
	v_lshlrev_b32_e32 v42, 16, v17
	v_and_b32_e32 v43, 0xffff0000, v17
	v_lshlrev_b32_e32 v44, 16, v18
	v_and_b32_e32 v45, 0xffff0000, v18
	v_lshlrev_b32_e32 v46, 16, v19
	v_and_b32_e32 v47, 0xffff0000, v19
	v_pk_fma_f32 v[40:41], v[196:197], v[204:205], v[40:41] op_sel_hi:[0,1,1] neg_lo:[0,0,1] neg_hi:[0,0,1]
	v_pk_fma_f32 v[42:43], v[196:197], v[206:207], v[42:43] op_sel_hi:[0,1,1] neg_lo:[0,0,1] neg_hi:[0,0,1]
	v_pk_fma_f32 v[44:45], v[196:197], v[208:209], v[44:45] op_sel_hi:[0,1,1] neg_lo:[0,0,1] neg_hi:[0,0,1]
	v_pk_fma_f32 v[46:47], v[196:197], v[210:211], v[46:47] op_sel_hi:[0,1,1] neg_lo:[0,0,1] neg_hi:[0,0,1]
	v_cvt_pk_bf16_f32 v218, v40, v41
	v_cvt_pk_bf16_f32 v219, v42, v43
	v_cvt_pk_bf16_f32 v220, v44, v45
	v_cvt_pk_bf16_f32 v221, v46, v47
	global_store_dwordx4 v12, v[218:221], s[24:25]
	v_add_u32_e32 v51, 14, v50
	v_add_u32_e32 v60, 0, v51
	v_min_u32_e32 v60, 64, v60
	v_lshl_add_u32 v60, v60, 10, v3
	ds_read_b128 v[204:207], v60
	ds_read_b128 v[208:211], v60 offset:16
	v_add_u32_e32 v60, 1, v51
	v_min_u32_e32 v60, 64, v60
	v_lshl_add_u32 v60, v60, 10, v3
	ds_read_b128 v[76:79], v60
	ds_read_b128 v[80:83], v60 offset:16
	v_add_u32_e32 v60, 2, v51
	v_min_u32_e32 v60, 64, v60
	v_lshl_add_u32 v60, v60, 10, v3
	ds_read_b128 v[84:87], v60
	ds_read_b128 v[88:91], v60 offset:16
	v_add_u32_e32 v60, 3, v51
	v_min_u32_e32 v60, 64, v60
	v_lshl_add_u32 v60, v60, 10, v3
	ds_read_b128 v[92:95], v60
	ds_read_b128 v[96:99], v60 offset:16
	s_waitcnt lgkmcnt(4)
; #define LAS __attribute__((address_space(3)))
; __device__ __forceinline__ unsigned pk2(float lo, float hi) { return f2bf(lo) | (f2bf(hi) << 16); }
; template <int HALFW>
; __device__ __forceinline__ void pool_item(const bf16* P, bf16* DP, LAS float* tmp, int tid, int b, int r, int g) {
;     ...
;     for (int q = 0; q < 4; ++q) { const int p = tid + 512 * q, c = p >> 5, ch0 = (p & 31) * 8;
;         const int clo = c - HALFW < 0 ? 0 : c - HALFW, chi = c + HALFW > 64 ? 64 : c + HALFW; const float cinv = 1.f / (float)(chi - clo);
;         const size_t o = ((size_t)(b * 2048 + r * 64 + c)) * 1024 + g * 256 + ch0;
;         const v4u x = *(const v4u*)(P + o);
;         f32x4 a0 = (f32x4){0.f, 0.f, 0.f, 0.f}, a1 = a0;
; #pragma unroll
;         for (int u = 0; u < 2 * HALFW; ++u) { const int cc = (clo + u < chi) ? clo + u : clo; const float m = (clo + u < chi) ? 1.f : 0.f;
;             a0 += *(const LAS f32x4*)(tmp + cc * 256 + ch0) * m; a1 += *(const LAS f32x4*)(tmp + cc * 256 + ch0 + 4) * m; }
;         v4u d; d.x = pk2(a0[0] * cinv - bflo(x.x), a0[1] * cinv - bfhi(x.x)); d.y = pk2(a0[2] * cinv - bflo(x.y), a0[3] * cinv - bfhi(x.y));
;         d.z = pk2(a1[0] * cinv - bflo(x.z), a1[1] * cinv - bfhi(x.z)); d.w = pk2(a1[2] * cinv - bflo(x.w), a1[3] * cinv - bfhi(x.w));
;         *(v4u*)(DP + o) = d; }
;     __syncthreads();
	v_pk_add_f32 v[204:205], v[204:205], v[76:77]
	v_pk_add_f32 v[206:207], v[206:207], v[78:79]
	v_pk_add_f32 v[208:209], v[208:209], v[80:81]
	v_pk_add_f32 v[210:211], v[210:211], v[82:83]
	s_waitcnt lgkmcnt(0)
	v_pk_add_f32 v[204:205], v[204:205], v[84:85]
	v_pk_add_f32 v[206:207], v[206:207], v[86:87]
	v_pk_add_f32 v[208:209], v[208:209], v[88:89]
	v_pk_add_f32 v[210:211], v[210:211], v[90:91]
	v_pk_add_f32 v[204:205], v[204:205], v[92:93]
	v_pk_add_f32 v[206:207], v[206:207], v[94:95]
	v_pk_add_f32 v[208:209], v[208:209], v[96:97]
	v_pk_add_f32 v[210:211], v[210:211], v[98:99]
	v_lshlrev_b32_e32 v40, 16, v20
	v_and_b32_e32 v41, 0xffff0000, v20
	v_lshlrev_b32_e32 v42, 16, v21
	v_and_b32_e32 v43, 0xffff0000, v21
	v_lshlrev_b32_e32 v44, 16, v22
	v_and_b32_e32 v45, 0xffff0000, v22
	v_lshlrev_b32_e32 v46, 16, v23
	v_and_b32_e32 v47, 0xffff0000, v23
	v_pk_fma_f32 v[40:41], v[198:199], v[204:205], v[40:41] op_sel_hi:[0,1,1] neg_lo:[0,0,1] neg_hi:[0,0,1]
	v_pk_fma_f32 v[42:43], v[198:199], v[206:207], v[42:43] op_sel_hi:[0,1,1] neg_lo:[0,0,1] neg_hi:[0,0,1]
	v_pk_fma_f32 v[44:45], v[198:199], v[208:209], v[44:45] op_sel_hi:[0,1,1] neg_lo:[0,0,1] neg_hi:[0,0,1]
	v_pk_fma_f32 v[46:47], v[198:199], v[210:211], v[46:47] op_sel_hi:[0,1,1] neg_lo:[0,0,1] neg_hi:[0,0,1]
	v_cvt_pk_bf16_f32 v222, v40, v41
	v_cvt_pk_bf16_f32 v223, v42, v43
	v_cvt_pk_bf16_f32 v224, v44, v45
	v_cvt_pk_bf16_f32 v225, v46, v47
	global_store_dwordx4 v13, v[222:225], s[24:25]
	v_add_u32_e32 v51, 30, v50
	v_add_u32_e32 v60, 0, v51
	v_min_u32_e32 v60, 64, v60
	v_lshl_add_u32 v60, v60, 10, v3
	ds_read_b128 v[204:207], v60
	ds_read_b128 v[208:211], v60 offset:16
	v_add_u32_e32 v60, 1, v51
	v_min_u32_e32 v60, 64, v60
	v_lshl_add_u32 v60, v60, 10, v3
	ds_read_b128 v[76:79], v60
	ds_read_b128 v[80:83], v60 offset:16
	v_add_u32_e32 v60, 2, v51
	v_min_u32_e32 v60, 64, v60
	v_lshl_add_u32 v60, v60, 10, v3
	ds_read_b128 v[84:87], v60
	ds_read_b128 v[88:91], v60 offset:16
	v_add_u32_e32 v60, 3, v51
	v_min_u32_e32 v60, 64, v60
	v_lshl_add_u32 v60, v60, 10, v3
	ds_read_b128 v[92:95], v60
	ds_read_b128 v[96:99], v60 offset:16
	s_waitcnt lgkmcnt(4)
	v_pk_add_f32 v[204:205], v[204:205], v[76:77]
	v_pk_add_f32 v[206:207], v[206:207], v[78:79]
	v_pk_add_f32 v[208:209], v[208:209], v[80:81]
	v_pk_add_f32 v[210:211], v[210:211], v[82:83]
	s_waitcnt lgkmcnt(0)
	v_pk_add_f32 v[204:205], v[204:205], v[84:85]
	v_pk_add_f32 v[206:207], v[206:207], v[86:87]
	v_pk_add_f32 v[208:209], v[208:209], v[88:89]
	v_pk_add_f32 v[210:211], v[210:211], v[90:91]
	v_pk_add_f32 v[204:205], v[204:205], v[92:93]
	v_pk_add_f32 v[206:207], v[206:207], v[94:95]
	v_pk_add_f32 v[208:209], v[208:209], v[96:97]
	v_pk_add_f32 v[210:211], v[210:211], v[98:99]
	v_lshlrev_b32_e32 v40, 16, v24
	v_and_b32_e32 v41, 0xffff0000, v24
	v_lshlrev_b32_e32 v42, 16, v25
	v_and_b32_e32 v43, 0xffff0000, v25
	v_lshlrev_b32_e32 v44, 16, v26
	v_and_b32_e32 v45, 0xffff0000, v26
	v_lshlrev_b32_e32 v46, 16, v27
	v_and_b32_e32 v47, 0xffff0000, v27
	v_pk_fma_f32 v[40:41], v[200:201], v[204:205], v[40:41] op_sel_hi:[0,1,1] neg_lo:[0,0,1] neg_hi:[0,0,1]
	v_pk_fma_f32 v[42:43], v[200:201], v[206:207], v[42:43] op_sel_hi:[0,1,1] neg_lo:[0,0,1] neg_hi:[0,0,1]
	v_pk_fma_f32 v[44:45], v[200:201], v[208:209], v[44:45] op_sel_hi:[0,1,1] neg_lo:[0,0,1] neg_hi:[0,0,1]
	v_pk_fma_f32 v[46:47], v[200:201], v[210:211], v[46:47] op_sel_hi:[0,1,1] neg_lo:[0,0,1] neg_hi:[0,0,1]
	v_cvt_pk_bf16_f32 v218, v40, v41
	v_cvt_pk_bf16_f32 v219, v42, v43
	v_cvt_pk_bf16_f32 v220, v44, v45
	v_cvt_pk_bf16_f32 v221, v46, v47
	global_store_dwordx4 v14, v[218:221], s[24:25]
	v_add_u32_e32 v51, 46, v50
	v_add_u32_e32 v60, 0, v51
	v_min_u32_e32 v60, 64, v60
	v_lshl_add_u32 v60, v60, 10, v3
	ds_read_b128 v[204:207], v60
	ds_read_b128 v[208:211], v60 offset:16
	v_add_u32_e32 v60, 1, v51
	v_min_u32_e32 v60, 64, v60
	v_lshl_add_u32 v60, v60, 10, v3
	ds_read_b128 v[76:79], v60
	ds_read_b128 v[80:83], v60 offset:16
	v_add_u32_e32 v60, 2, v51
	v_min_u32_e32 v60, 64, v60
	v_lshl_add_u32 v60, v60, 10, v3
	ds_read_b128 v[84:87], v60
	ds_read_b128 v[88:91], v60 offset:16
	v_add_u32_e32 v60, 3, v51
	v_min_u32_e32 v60, 64, v60
	v_lshl_add_u32 v60, v60, 10, v3
	ds_read_b128 v[92:95], v60
	ds_read_b128 v[96:99], v60 offset:16
	s_waitcnt lgkmcnt(4)
	v_pk_add_f32 v[204:205], v[204:205], v[76:77]
	v_pk_add_f32 v[206:207], v[206:207], v[78:79]
	v_pk_add_f32 v[208:209], v[208:209], v[80:81]
	v_pk_add_f32 v[210:211], v[210:211], v[82:83]
	s_waitcnt lgkmcnt(0)
	v_pk_add_f32 v[204:205], v[204:205], v[84:85]
	v_pk_add_f32 v[206:207], v[206:207], v[86:87]
	v_pk_add_f32 v[208:209], v[208:209], v[88:89]
	v_pk_add_f32 v[210:211], v[210:211], v[90:91]
	v_pk_add_f32 v[204:205], v[204:205], v[92:93]
	v_pk_add_f32 v[206:207], v[206:207], v[94:95]
	v_pk_add_f32 v[208:209], v[208:209], v[96:97]
	v_pk_add_f32 v[210:211], v[210:211], v[98:99]
	v_lshlrev_b32_e32 v40, 16, v28
	v_and_b32_e32 v41, 0xffff0000, v28
	v_lshlrev_b32_e32 v42, 16, v29
	v_and_b32_e32 v43, 0xffff0000, v29
	v_lshlrev_b32_e32 v44, 16, v30
	v_and_b32_e32 v45, 0xffff0000, v30
	v_lshlrev_b32_e32 v46, 16, v31
	v_and_b32_e32 v47, 0xffff0000, v31
	v_pk_fma_f32 v[40:41], v[202:203], v[204:205], v[40:41] op_sel_hi:[0,1,1] neg_lo:[0,0,1] neg_hi:[0,0,1]
	v_pk_fma_f32 v[42:43], v[202:203], v[206:207], v[42:43] op_sel_hi:[0,1,1] neg_lo:[0,0,1] neg_hi:[0,0,1]
	v_pk_fma_f32 v[44:45], v[202:203], v[208:209], v[44:45] op_sel_hi:[0,1,1] neg_lo:[0,0,1] neg_hi:[0,0,1]
	v_pk_fma_f32 v[46:47], v[202:203], v[210:211], v[46:47] op_sel_hi:[0,1,1] neg_lo:[0,0,1] neg_hi:[0,0,1]
	v_cvt_pk_bf16_f32 v222, v40, v41
	v_cvt_pk_bf16_f32 v223, v42, v43
	v_cvt_pk_bf16_f32 v224, v44, v45
	v_cvt_pk_bf16_f32 v225, v46, v47
	global_store_dwordx4 v15, v[222:225], s[24:25]
	s_barrier
	s_branch .LBB0_678

; #define LAS __attribute__((address_space(3)))
; template <int HALFW>
; __device__ __forceinline__ void pool_item(const bf16* P, bf16* DP, LAS float* tmp, int tid, int b, int r, int g) {
;     ...
;         *(LAS f32x4*)(tmp + c * 256 + ch0) = (f32x4){acc[0] * rinv, acc[1] * rinv, acc[2] * rinv, acc[3] * rinv};
;         *(LAS f32x4*)(tmp + c * 256 + ch0 + 4) = (f32x4){acc[4] * rinv, acc[5] * rinv, acc[6] * rinv, acc[7] * rinv}; }
;     __syncthreads();
; #pragma unroll 1
;     for (int q = 0; q < 4; ++q) { const int p = tid + 512 * q, c = p >> 5, ch0 = (p & 31) * 8;
;         const int clo = c - HALFW < 0 ? 0 : c - HALFW, chi = c + HALFW > 64 ? 64 : c + HALFW; const float cinv = 1.f / (float)(chi - clo);
;         const size_t o = ((size_t)(b * 2048 + r * 64 + c)) * 1024 + g * 256 + ch0;
;         const v4u x = *(const v4u*)(P + o);
;         f32x4 a0 = (f32x4){0.f, 0.f, 0.f, 0.f}, a1 = a0;
; #pragma unroll
;         for (int u = 0; u < 2 * HALFW; ++u) { const int cc = (clo + u < chi) ? clo + u : clo; const float m = (clo + u < chi) ? 1.f : 0.f;
;             a0 += *(const LAS f32x4*)(tmp + cc * 256 + ch0) * m; a1 += *(const LAS f32x4*)(tmp + cc * 256 + ch0 + 4) * m; }
.Lpool_h4_q3:
	v_pk_mul_f32 v[52:53], v[52:53], v[48:49] op_sel_hi:[1,0]
	v_pk_mul_f32 v[54:55], v[54:55], v[48:49] op_sel_hi:[1,0]
	v_pk_mul_f32 v[56:57], v[56:57], v[48:49] op_sel_hi:[1,0]
	v_pk_mul_f32 v[58:59], v[58:59], v[48:49] op_sel_hi:[1,0]
	ds_write_b128 v49, v[52:55] offset:49152
	ds_write_b128 v49, v[56:59] offset:49168
	v_add_u32_e32 v51, 0, v50
	v_add_u32_e32 v60, 4, v51
	v_min_u32_e32 v60, 64, v60
	v_sub_u32_e64 v61, v51, 4 clamp
	v_sub_u32_e32 v60, v60, v61
	v_cvt_f32_u32_e32 v212, v60
	v_div_scale_f32 v213, s[30:31], v212, v212, 1.0
	v_div_scale_f32 v215, vcc, 1.0, v212, 1.0
	v_rcp_f32_e32 v214, v213
	s_nop 1
	v_fma_f32 v216, -v213, v214, 1.0
	v_fmac_f32_e32 v214, v216, v214
	v_mul_f32_e32 v216, v215, v214
	v_fma_f32 v217, -v213, v216, v215
	v_fmac_f32_e32 v216, v217, v214
	v_fma_f32 v213, -v213, v216, v215
	s_nop 1
	v_div_fmas_f32 v213, v213, v214, v216
	v_div_fixup_f32 v196, v213, v212, 1.0
	v_add_u32_e32 v51, 16, v50
	v_add_u32_e32 v60, 4, v51
	v_min_u32_e32 v60, 64, v60
	v_sub_u32_e64 v61, v51, 4 clamp
	v_sub_u32_e32 v60, v60, v61
	v_cvt_f32_u32_e32 v212, v60
	v_div_scale_f32 v213, s[30:31], v212, v212, 1.0
	v_div_scale_f32 v215, vcc, 1.0, v212, 1.0
	v_rcp_f32_e32 v214, v213
	s_nop 1
	v_fma_f32 v216, -v213, v214, 1.0
	v_fmac_f32_e32 v214, v216, v214
	v_mul_f32_e32 v216, v215, v214
	v_fma_f32 v217, -v213, v216, v215
	v_fmac_f32_e32 v216, v217, v214
	v_fma_f32 v213, -v213, v216, v215
	s_nop 1
	v_div_fmas_f32 v213, v213, v214, v216
	v_div_fixup_f32 v198, v213, v212, 1.0
	v_add_u32_e32 v51, 32, v50
	v_add_u32_e32 v60, 4, v51
	v_min_u32_e32 v60, 64, v60
	v_sub_u32_e64 v61, v51, 4 clamp
	v_sub_u32_e32 v60, v60, v61
	v_cvt_f32_u32_e32 v212, v60
	v_div_scale_f32 v213, s[30:31], v212, v212, 1.0
	v_div_scale_f32 v215, vcc, 1.0, v212, 1.0
	v_rcp_f32_e32 v214, v213
	s_nop 1
	v_fma_f32 v216, -v213, v214, 1.0
	v_fmac_f32_e32 v214, v216, v214
	v_mul_f32_e32 v216, v215, v214
	v_fma_f32 v217, -v213, v216, v215
	v_fmac_f32_e32 v216, v217, v214
	v_fma_f32 v213, -v213, v216, v215
	s_nop 1
	v_div_fmas_f32 v213, v213, v214, v216
	v_div_fixup_f32 v200, v213, v212, 1.0
	v_add_u32_e32 v51, 48, v50
	v_add_u32_e32 v60, 4, v51
	v_min_u32_e32 v60, 64, v60
	v_sub_u32_e64 v61, v51, 4 clamp
	v_sub_u32_e32 v60, v60, v61
	v_cvt_f32_u32_e32 v212, v60
	v_div_scale_f32 v213, s[30:31], v212, v212, 1.0
	v_div_scale_f32 v215, vcc, 1.0, v212, 1.0
	v_rcp_f32_e32 v214, v213
	s_nop 1
	v_fma_f32 v216, -v213, v214, 1.0
	v_fmac_f32_e32 v214, v216, v214
	v_mul_f32_e32 v216, v215, v214
	v_fma_f32 v217, -v213, v216, v215
	v_fmac_f32_e32 v216, v217, v214
	v_fma_f32 v213, -v213, v216, v215
	s_nop 1
	v_div_fmas_f32 v213, v213, v214, v216
	v_div_fixup_f32 v202, v213, v212, 1.0
	s_waitcnt lgkmcnt(0)
	s_barrier
	v_add_u32_e32 v51, -4, v50
	v_add_u32_e32 v60, 0, v51
	v_min_u32_e32 v60, 64, v60
	v_lshl_add_u32 v60, v60, 10, v3
	ds_read_b128 v[204:207], v60
	ds_read_b128 v[208:211], v60 offset:16
	v_add_u32_e32 v60, 1, v51
	v_min_u32_e32 v60, 64, v60
	v_lshl_add_u32 v60, v60, 10, v3
	ds_read_b128 v[76:79], v60
	ds_read_b128 v[80:83], v60 offset:16
	v_add_u32_e32 v60, 2, v51
	v_min_u32_e32 v60, 64, v60
	v_lshl_add_u32 v60, v60, 10, v3
	ds_read_b128 v[84:87], v60
	ds_read_b128 v[88:91], v60 offset:16
	v_add_u32_e32 v60, 3, v51
	v_min_u32_e32 v60, 64, v60
	v_lshl_add_u32 v60, v60, 10, v3
	ds_read_b128 v[92:95], v60
	ds_read_b128 v[96:99], v60 offset:16
	v_add_u32_e32 v60, 4, v51
	v_min_u32_e32 v60, 64, v60
	v_lshl_add_u32 v60, v60, 10, v3
	ds_read_b128 v[100:103], v60
	ds_read_b128 v[104:107], v60 offset:16
	v_add_u32_e32 v60, 5, v51
	v_min_u32_e32 v60, 64, v60
	v_lshl_add_u32 v60, v60, 10, v3
	ds_read_b128 v[108:111], v60
	ds_read_b128 v[112:115], v60 offset:16
	s_waitcnt lgkmcnt(8)
	v_pk_add_f32 v[204:205], v[204:205], v[76:77]
	v_pk_add_f32 v[206:207], v[206:207], v[78:79]
	v_pk_add_f32 v[208:209], v[208:209], v[80:81]
	v_pk_add_f32 v[210:211], v[210:211], v[82:83]
	v_add_u32_e32 v60, 6, v51
	v_min_u32_e32 v60, 64, v60
	v_lshl_add_u32 v60, v60, 10, v3
	ds_read_b128 v[68:71], v60
	ds_read_b128 v[72:75], v60 offset:16
	v_add_u32_e32 v60, 7, v51
	v_min_u32_e32 v60, 64, v60
	v_lshl_add_u32 v60, v60, 10, v3
	ds_read_b128 v[76:79], v60
	ds_read_b128 v[80:83], v60 offset:16
	s_waitcnt lgkmcnt(8)
	v_pk_add_f32 v[204:205], v[204:205], v[84:85]
	v_pk_add_f32 v[206:207], v[206:207], v[86:87]
	v_pk_add_f32 v[208:209], v[208:209], v[88:89]
	v_pk_add_f32 v[210:211], v[210:211], v[90:91]
	v_pk_add_f32 v[204:205], v[204:205], v[92:93]
	v_pk_add_f32 v[206:207], v[206:207], v[94:95]
	v_pk_add_f32 v[208:209], v[208:209], v[96:97]
	v_pk_add_f32 v[210:211], v[210:211], v[98:99]
	s_waitcnt lgkmcnt(4)
	v_pk_add_f32 v[204:205], v[204:205], v[100:101]
	v_pk_add_f32 v[206:207], v[206:207], v[102:103]
	v_pk_add_f32 v[208:209], v[208:209], v[104:105]
	v_pk_add_f32 v[210:211], v[210:211], v[106:107]
	v_pk_add_f32 v[204:205], v[204:205], v[108:109]
	v_pk_add_f32 v[206:207], v[206:207], v[110:111]
	v_pk_add_f32 v[208:209], v[208:209], v[112:113]
	v_pk_add_f32 v[210:211], v[210:211], v[114:115]
	s_waitcnt lgkmcnt(0)
	v_pk_add_f32 v[204:205], v[204:205], v[68:69]
	v_pk_add_f32 v[206:207], v[206:207], v[70:71]
	v_pk_add_f32 v[208:209], v[208:209], v[72:73]
	v_pk_add_f32 v[210:211], v[210:211], v[74:75]
	v_pk_add_f32 v[204:205], v[204:205], v[76:77]
	v_pk_add_f32 v[206:207], v[206:207], v[78:79]
	v_pk_add_f32 v[208:209], v[208:209], v[80:81]
	v_pk_add_f32 v[210:211], v[210:211], v[82:83]
	s_waitcnt vmcnt(0)
; #define LAS __attribute__((address_space(3)))
; __device__ __forceinline__ unsigned pk2(float lo, float hi) { return f2bf(lo) | (f2bf(hi) << 16); }
; template <int HALFW>
; __device__ __forceinline__ void pool_item(const bf16* P, bf16* DP, LAS float* tmp, int tid, int b, int r, int g) {
;     const int rlo = r - HALFW < 0 ? 0 : r - HALFW, rhi = r + HALFW > 32 ? 32 : r + HALFW;
;     const float rinv = 1.f / (float)(rhi - rlo);
; #pragma unroll 1
;     for (int q = 0; q < 4; ++q) { const int p = tid + 512 * q, c = p >> 5, ch0 = (p & 31) * 8; float acc[8]; v4u x[2 * HALFW];
; #pragma unroll
;         for (int u = 0; u < 2 * HALFW; ++u) { const int rr = (rlo + u < rhi) ? rlo + u : rlo; x[u] = *(const v4u*)(P + ((size_t)(b * 2048 + rr * 64 + c)) * 1024 + g * 256 + ch0); }
;     ...
;     for (int q = 0; q < 4; ++q) { const int p = tid + 512 * q, c = p >> 5, ch0 = (p & 31) * 8;
;         const int clo = c - HALFW < 0 ? 0 : c - HALFW, chi = c + HALFW > 64 ? 64 : c + HALFW; const float cinv = 1.f / (float)(chi - clo);
;         const size_t o = ((size_t)(b * 2048 + r * 64 + c)) * 1024 + g * 256 + ch0;
;         const v4u x = *(const v4u*)(P + o);
;         f32x4 a0 = (f32x4){0.f, 0.f, 0.f, 0.f}, a1 = a0;
; #pragma unroll
;         for (int u = 0; u < 2 * HALFW; ++u) { const int cc = (clo + u < chi) ? clo + u : clo; const float m = (clo + u < chi) ? 1.f : 0.f;
;             a0 += *(const LAS f32x4*)(tmp + cc * 256 + ch0) * m; a1 += *(const LAS f32x4*)(tmp + cc * 256 + ch0 + 4) * m; }
;         v4u d; d.x = pk2(a0[0] * cinv - bflo(x.x), a0[1] * cinv - bfhi(x.x)); d.y = pk2(a0[2] * cinv - bflo(x.y), a0[3] * cinv - bfhi(x.y));
;         d.z = pk2(a1[0] * cinv - bflo(x.z), a1[1] * cinv - bfhi(x.z)); d.w = pk2(a1[2] * cinv - bflo(x.w), a1[3] * cinv - bfhi(x.w));
;         *(v4u*)(DP + o) = d; }
	s_sub_i32 s39, s37, 2
	s_max_i32 s39, s39, 0
	s_add_i32 s40, s37, 2
	s_min_i32 s40, s40, 32
	s_sub_i32 s41, s40, s39
	s_add_i32 s41, s41, -1
	s_lshl_b32 s39, s39, 6
	s_add_i32 s39, s29, s39
	s_lshl_b32 s39, s39, 11
	s_add_u32 s50, s44, s39
	s_addc_u32 s51, s45, 0
	s_add_u32 s50, s50, 512
	s_addc_u32 s51, s51, 0
	v_lshrrev_b32_e32 v240, 8, v66
	v_bfe_u32 v241, v66, 2, 6
	v_and_b32_e32 v242, 3, v66
	v_lshlrev_b32_e32 v241, 11, v241
	v_lshl_or_b32 v241, v242, 7, v241
	v_min_u32_e32 v242, s41, v240
	v_lshl_add_u32 v243, v242, 17, v241
	global_load_dword v244, v243, s[50:51]
	v_add_u32_e32 v242, 2, v240
	v_min_u32_e32 v242, s41, v242
	v_lshl_add_u32 v243, v242, 17, v241
	global_load_dword v244, v243, s[50:51]
	v_lshlrev_b32_e32 v40, 16, v16
	v_and_b32_e32 v41, 0xffff0000, v16
	v_lshlrev_b32_e32 v42, 16, v17
	v_and_b32_e32 v43, 0xffff0000, v17
	v_lshlrev_b32_e32 v44, 16, v18
	v_and_b32_e32 v45, 0xffff0000, v18
	v_lshlrev_b32_e32 v46, 16, v19
	v_and_b32_e32 v47, 0xffff0000, v19
	v_pk_fma_f32 v[40:41], v[196:197], v[204:205], v[40:41] op_sel_hi:[0,1,1] neg_lo:[0,0,1] neg_hi:[0,0,1]
	v_pk_fma_f32 v[42:43], v[196:197], v[206:207], v[42:43] op_sel_hi:[0,1,1] neg_lo:[0,0,1] neg_hi:[0,0,1]
	v_pk_fma_f32 v[44:45], v[196:197], v[208:209], v[44:45] op_sel_hi:[0,1,1] neg_lo:[0,0,1] neg_hi:[0,0,1]
	v_pk_fma_f32 v[46:47], v[196:197], v[210:211], v[46:47] op_sel_hi:[0,1,1] neg_lo:[0,0,1] neg_hi:[0,0,1]
	v_cvt_pk_bf16_f32 v218, v40, v41
	v_cvt_pk_bf16_f32 v219, v42, v43
	v_cvt_pk_bf16_f32 v220, v44, v45
	v_cvt_pk_bf16_f32 v221, v46, v47
	global_store_dwordx4 v12, v[218:221], s[24:25]
	v_add_u32_e32 v51, 12, v50
	v_add_u32_e32 v60, 0, v51
	v_min_u32_e32 v60, 64, v60
	v_lshl_add_u32 v60, v60, 10, v3
	ds_read_b128 v[204:207], v60
	ds_read_b128 v[208:211], v60 offset:16
	v_add_u32_e32 v60, 1, v51
	v_min_u32_e32 v60, 64, v60
	v_lshl_add_u32 v60, v60, 10, v3
	ds_read_b128 v[76:79], v60
	ds_read_b128 v[80:83], v60 offset:16
	v_add_u32_e32 v60, 2, v51
	v_min_u32_e32 v60, 64, v60
	v_lshl_add_u32 v60, v60, 10, v3
	ds_read_b128 v[84:87], v60
	ds_read_b128 v[88:91], v60 offset:16
	v_add_u32_e32 v60, 3, v51
	v_min_u32_e32 v60, 64, v60
	v_lshl_add_u32 v60, v60, 10, v3
	ds_read_b128 v[92:95], v60
	ds_read_b128 v[96:99], v60 offset:16
	v_add_u32_e32 v60, 4, v51
	v_min_u32_e32 v60, 64, v60
	v_lshl_add_u32 v60, v60, 10, v3
	ds_read_b128 v[100:103], v60
	ds_read_b128 v[104:107], v60 offset:16
	v_add_u32_e32 v60, 5, v51
	v_min_u32_e32 v60, 64, v60
	v_lshl_add_u32 v60, v60, 10, v3
	ds_read_b128 v[108:111], v60
	ds_read_b128 v[112:115], v60 offset:16
	s_waitcnt lgkmcnt(8)
	v_pk_add_f32 v[204:205], v[204:205], v[76:77]
	v_pk_add_f32 v[206:207], v[206:207], v[78:79]
	v_pk_add_f32 v[208:209], v[208:209], v[80:81]
	v_pk_add_f32 v[210:211], v[210:211], v[82:83]
	v_add_u32_e32 v60, 6, v51
	v_min_u32_e32 v60, 64, v60
	v_lshl_add_u32 v60, v60, 10, v3
	ds_read_b128 v[68:71], v60
	ds_read_b128 v[72:75], v60 offset:16
	v_add_u32_e32 v60, 7, v51
	v_min_u32_e32 v60, 64, v60
	v_lshl_add_u32 v60, v60, 10, v3
	ds_read_b128 v[76:79], v60
	ds_read_b128 v[80:83], v60 offset:16
	s_waitcnt lgkmcnt(8)
	v_pk_add_f32 v[204:205], v[204:205], v[84:85]
	v_pk_add_f32 v[206:207], v[206:207], v[86:87]
	v_pk_add_f32 v[208:209], v[208:209], v[88:89]
	v_pk_add_f32 v[210:211], v[210:211], v[90:91]
	v_pk_add_f32 v[204:205], v[204:205], v[92:93]
	v_pk_add_f32 v[206:207], v[206:207], v[94:95]
	v_pk_add_f32 v[208:209], v[208:209], v[96:97]
	v_pk_add_f32 v[210:211], v[210:211], v[98:99]
	s_waitcnt lgkmcnt(4)
	v_pk_add_f32 v[204:205], v[204:205], v[100:101]
	v_pk_add_f32 v[206:207], v[206:207], v[102:103]
	v_pk_add_f32 v[208:209], v[208:209], v[104:105]
	v_pk_add_f32 v[210:211], v[210:211], v[106:107]
	v_pk_add_f32 v[204:205], v[204:205], v[108:109]
	v_pk_add_f32 v[206:207], v[206:207], v[110:111]
	v_pk_add_f32 v[208:209], v[208:209], v[112:113]
	v_pk_add_f32 v[210:211], v[210:211], v[114:115]
	s_waitcnt lgkmcnt(0)
	v_pk_add_f32 v[204:205], v[204:205], v[68:69]
	v_pk_add_f32 v[206:207], v[206:207], v[70:71]
	v_pk_add_f32 v[208:209], v[208:209], v[72:73]
	v_pk_add_f32 v[210:211], v[210:211], v[74:75]
	v_pk_add_f32 v[204:205], v[204:205], v[76:77]
	v_pk_add_f32 v[206:207], v[206:207], v[78:79]
	v_pk_add_f32 v[208:209], v[208:209], v[80:81]
	v_pk_add_f32 v[210:211], v[210:211], v[82:83]
	v_lshlrev_b32_e32 v40, 16, v20
	v_and_b32_e32 v41, 0xffff0000, v20
	v_lshlrev_b32_e32 v42, 16, v21
	v_and_b32_e32 v43, 0xffff0000, v21
	v_lshlrev_b32_e32 v44, 16, v22
	v_and_b32_e32 v45, 0xffff0000, v22
	v_lshlrev_b32_e32 v46, 16, v23
	v_and_b32_e32 v47, 0xffff0000, v23
	v_pk_fma_f32 v[40:41], v[198:199], v[204:205], v[40:41] op_sel_hi:[0,1,1] neg_lo:[0,0,1] neg_hi:[0,0,1]
	v_pk_fma_f32 v[42:43], v[198:199], v[206:207], v[42:43] op_sel_hi:[0,1,1] neg_lo:[0,0,1] neg_hi:[0,0,1]
	v_pk_fma_f32 v[44:45], v[198:199], v[208:209], v[44:45] op_sel_hi:[0,1,1] neg_lo:[0,0,1] neg_hi:[0,0,1]
	v_pk_fma_f32 v[46:47], v[198:199], v[210:211], v[46:47] op_sel_hi:[0,1,1] neg_lo:[0,0,1] neg_hi:[0,0,1]
	v_cvt_pk_bf16_f32 v222, v40, v41
	v_cvt_pk_bf16_f32 v223, v42, v43
	v_cvt_pk_bf16_f32 v224, v44, v45
	v_cvt_pk_bf16_f32 v225, v46, v47
	global_store_dwordx4 v13, v[222:225], s[24:25]
	v_add_u32_e32 v51, 28, v50
	v_add_u32_e32 v60, 0, v51
	v_min_u32_e32 v60, 64, v60
	v_lshl_add_u32 v60, v60, 10, v3
	ds_read_b128 v[204:207], v60
	ds_read_b128 v[208:211], v60 offset:16
	v_add_u32_e32 v60, 1, v51
	v_min_u32_e32 v60, 64, v60
	v_lshl_add_u32 v60, v60, 10, v3
	ds_read_b128 v[76:79], v60
	ds_read_b128 v[80:83], v60 offset:16
	v_add_u32_e32 v60, 2, v51
	v_min_u32_e32 v60, 64, v60
	v_lshl_add_u32 v60, v60, 10, v3
	ds_read_b128 v[84:87], v60
	ds_read_b128 v[88:91], v60 offset:16
	v_add_u32_e32 v60, 3, v51
	v_min_u32_e32 v60, 64, v60
	v_lshl_add_u32 v60, v60, 10, v3
	ds_read_b128 v[92:95], v60
	ds_read_b128 v[96:99], v60 offset:16
	v_add_u32_e32 v60, 4, v51
	v_min_u32_e32 v60, 64, v60
	v_lshl_add_u32 v60, v60, 10, v3
	ds_read_b128 v[100:103], v60
	ds_read_b128 v[104:107], v60 offset:16
	v_add_u32_e32 v60, 5, v51
	v_min_u32_e32 v60, 64, v60
	v_lshl_add_u32 v60, v60, 10, v3
	ds_read_b128 v[108:111], v60
	ds_read_b128 v[112:115], v60 offset:16
	s_waitcnt lgkmcnt(8)
; #define LAS __attribute__((address_space(3)))
; __device__ __forceinline__ unsigned pk2(float lo, float hi) { return f2bf(lo) | (f2bf(hi) << 16); }
; template <int HALFW>
; __device__ __forceinline__ void pool_item(const bf16* P, bf16* DP, LAS float* tmp, int tid, int b, int r, int g) {
;     ...
;     for (int q = 0; q < 4; ++q) { const int p = tid + 512 * q, c = p >> 5, ch0 = (p & 31) * 8;
;         const int clo = c - HALFW < 0 ? 0 : c - HALFW, chi = c + HALFW > 64 ? 64 : c + HALFW; const float cinv = 1.f / (float)(chi - clo);
;         const size_t o = ((size_t)(b * 2048 + r * 64 + c)) * 1024 + g * 256 + ch0;
;         const v4u x = *(const v4u*)(P + o);
;         f32x4 a0 = (f32x4){0.f, 0.f, 0.f, 0.f}, a1 = a0;
; #pragma unroll
;         for (int u = 0; u < 2 * HALFW; ++u) { const int cc = (clo + u < chi) ? clo + u : clo; const float m = (clo + u < chi) ? 1.f : 0.f;
;             a0 += *(const LAS f32x4*)(tmp + cc * 256 + ch0) * m; a1 += *(const LAS f32x4*)(tmp + cc * 256 + ch0 + 4) * m; }
;         v4u d; d.x = pk2(a0[0] * cinv - bflo(x.x), a0[1] * cinv - bfhi(x.x)); d.y = pk2(a0[2] * cinv - bflo(x.y), a0[3] * cinv - bfhi(x.y));
;         d.z = pk2(a1[0] * cinv - bflo(x.z), a1[1] * cinv - bfhi(x.z)); d.w = pk2(a1[2] * cinv - bflo(x.w), a1[3] * cinv - bfhi(x.w));
;         *(v4u*)(DP + o) = d; }
;     __syncthreads();
	v_pk_add_f32 v[204:205], v[204:205], v[76:77]
	v_pk_add_f32 v[206:207], v[206:207], v[78:79]
	v_pk_add_f32 v[208:209], v[208:209], v[80:81]
	v_pk_add_f32 v[210:211], v[210:211], v[82:83]
	v_add_u32_e32 v60, 6, v51
	v_min_u32_e32 v60, 64, v60
	v_lshl_add_u32 v60, v60, 10, v3
	ds_read_b128 v[68:71], v60
	ds_read_b128 v[72:75], v60 offset:16
	v_add_u32_e32 v60, 7, v51
	v_min_u32_e32 v60, 64, v60
	v_lshl_add_u32 v60, v60, 10, v3
	ds_read_b128 v[76:79], v60
	ds_read_b128 v[80:83], v60 offset:16
	s_waitcnt lgkmcnt(8)
	v_pk_add_f32 v[204:205], v[204:205], v[84:85]
	v_pk_add_f32 v[206:207], v[206:207], v[86:87]
	v_pk_add_f32 v[208:209], v[208:209], v[88:89]
	v_pk_add_f32 v[210:211], v[210:211], v[90:91]
	v_pk_add_f32 v[204:205], v[204:205], v[92:93]
	v_pk_add_f32 v[206:207], v[206:207], v[94:95]
	v_pk_add_f32 v[208:209], v[208:209], v[96:97]
	v_pk_add_f32 v[210:211], v[210:211], v[98:99]
	s_waitcnt lgkmcnt(4)
	v_pk_add_f32 v[204:205], v[204:205], v[100:101]
	v_pk_add_f32 v[206:207], v[206:207], v[102:103]
	v_pk_add_f32 v[208:209], v[208:209], v[104:105]
	v_pk_add_f32 v[210:211], v[210:211], v[106:107]
	v_pk_add_f32 v[204:205], v[204:205], v[108:109]
	v_pk_add_f32 v[206:207], v[206:207], v[110:111]
	v_pk_add_f32 v[208:209], v[208:209], v[112:113]
	v_pk_add_f32 v[210:211], v[210:211], v[114:115]
	s_waitcnt lgkmcnt(0)
	v_pk_add_f32 v[204:205], v[204:205], v[68:69]
	v_pk_add_f32 v[206:207], v[206:207], v[70:71]
	v_pk_add_f32 v[208:209], v[208:209], v[72:73]
	v_pk_add_f32 v[210:211], v[210:211], v[74:75]
	v_pk_add_f32 v[204:205], v[204:205], v[76:77]
	v_pk_add_f32 v[206:207], v[206:207], v[78:79]
	v_pk_add_f32 v[208:209], v[208:209], v[80:81]
	v_pk_add_f32 v[210:211], v[210:211], v[82:83]
	v_lshlrev_b32_e32 v40, 16, v24
	v_and_b32_e32 v41, 0xffff0000, v24
	v_lshlrev_b32_e32 v42, 16, v25
	v_and_b32_e32 v43, 0xffff0000, v25
	v_lshlrev_b32_e32 v44, 16, v26
	v_and_b32_e32 v45, 0xffff0000, v26
	v_lshlrev_b32_e32 v46, 16, v27
	v_and_b32_e32 v47, 0xffff0000, v27
	v_pk_fma_f32 v[40:41], v[200:201], v[204:205], v[40:41] op_sel_hi:[0,1,1] neg_lo:[0,0,1] neg_hi:[0,0,1]
	v_pk_fma_f32 v[42:43], v[200:201], v[206:207], v[42:43] op_sel_hi:[0,1,1] neg_lo:[0,0,1] neg_hi:[0,0,1]
	v_pk_fma_f32 v[44:45], v[200:201], v[208:209], v[44:45] op_sel_hi:[0,1,1] neg_lo:[0,0,1] neg_hi:[0,0,1]
	v_pk_fma_f32 v[46:47], v[200:201], v[210:211], v[46:47] op_sel_hi:[0,1,1] neg_lo:[0,0,1] neg_hi:[0,0,1]
	v_cvt_pk_bf16_f32 v218, v40, v41
	v_cvt_pk_bf16_f32 v219, v42, v43
	v_cvt_pk_bf16_f32 v220, v44, v45
	v_cvt_pk_bf16_f32 v221, v46, v47
	global_store_dwordx4 v14, v[218:221], s[24:25]
	v_add_u32_e32 v51, 44, v50
	v_add_u32_e32 v60, 0, v51
	v_min_u32_e32 v60, 64, v60
	v_lshl_add_u32 v60, v60, 10, v3
	ds_read_b128 v[204:207], v60
	ds_read_b128 v[208:211], v60 offset:16
	v_add_u32_e32 v60, 1, v51
	v_min_u32_e32 v60, 64, v60
	v_lshl_add_u32 v60, v60, 10, v3
	ds_read_b128 v[76:79], v60
	ds_read_b128 v[80:83], v60 offset:16
	v_add_u32_e32 v60, 2, v51
	v_min_u32_e32 v60, 64, v60
	v_lshl_add_u32 v60, v60, 10, v3
	ds_read_b128 v[84:87], v60
	ds_read_b128 v[88:91], v60 offset:16
	v_add_u32_e32 v60, 3, v51
	v_min_u32_e32 v60, 64, v60
	v_lshl_add_u32 v60, v60, 10, v3
	ds_read_b128 v[92:95], v60
	ds_read_b128 v[96:99], v60 offset:16
	v_add_u32_e32 v60, 4, v51
	v_min_u32_e32 v60, 64, v60
	v_lshl_add_u32 v60, v60, 10, v3
	ds_read_b128 v[100:103], v60
	ds_read_b128 v[104:107], v60 offset:16
	v_add_u32_e32 v60, 5, v51
	v_min_u32_e32 v60, 64, v60
	v_lshl_add_u32 v60, v60, 10, v3
	ds_read_b128 v[108:111], v60
	ds_read_b128 v[112:115], v60 offset:16
	s_waitcnt lgkmcnt(8)
	v_pk_add_f32 v[204:205], v[204:205], v[76:77]
	v_pk_add_f32 v[206:207], v[206:207], v[78:79]
	v_pk_add_f32 v[208:209], v[208:209], v[80:81]
	v_pk_add_f32 v[210:211], v[210:211], v[82:83]
	v_add_u32_e32 v60, 6, v51
	v_min_u32_e32 v60, 64, v60
	v_lshl_add_u32 v60, v60, 10, v3
	ds_read_b128 v[68:71], v60
	ds_read_b128 v[72:75], v60 offset:16
	v_add_u32_e32 v60, 7, v51
	v_min_u32_e32 v60, 64, v60
	v_lshl_add_u32 v60, v60, 10, v3
	ds_read_b128 v[76:79], v60
	ds_read_b128 v[80:83], v60 offset:16
	s_waitcnt lgkmcnt(8)
	v_pk_add_f32 v[204:205], v[204:205], v[84:85]
	v_pk_add_f32 v[206:207], v[206:207], v[86:87]
	v_pk_add_f32 v[208:209], v[208:209], v[88:89]
	v_pk_add_f32 v[210:211], v[210:211], v[90:91]
	v_pk_add_f32 v[204:205], v[204:205], v[92:93]
	v_pk_add_f32 v[206:207], v[206:207], v[94:95]
	v_pk_add_f32 v[208:209], v[208:209], v[96:97]
	v_pk_add_f32 v[210:211], v[210:211], v[98:99]
	s_waitcnt lgkmcnt(4)
	v_pk_add_f32 v[204:205], v[204:205], v[100:101]
	v_pk_add_f32 v[206:207], v[206:207], v[102:103]
	v_pk_add_f32 v[208:209], v[208:209], v[104:105]
	v_pk_add_f32 v[210:211], v[210:211], v[106:107]
	v_pk_add_f32 v[204:205], v[204:205], v[108:109]
	v_pk_add_f32 v[206:207], v[206:207], v[110:111]
	v_pk_add_f32 v[208:209], v[208:209], v[112:113]
	v_pk_add_f32 v[210:211], v[210:211], v[114:115]
	s_waitcnt lgkmcnt(0)
	v_pk_add_f32 v[204:205], v[204:205], v[68:69]
	v_pk_add_f32 v[206:207], v[206:207], v[70:71]
	v_pk_add_f32 v[208:209], v[208:209], v[72:73]
	v_pk_add_f32 v[210:211], v[210:211], v[74:75]
	v_pk_add_f32 v[204:205], v[204:205], v[76:77]
	v_pk_add_f32 v[206:207], v[206:207], v[78:79]
	v_pk_add_f32 v[208:209], v[208:209], v[80:81]
	v_pk_add_f32 v[210:211], v[210:211], v[82:83]
	v_lshlrev_b32_e32 v40, 16, v28
	v_and_b32_e32 v41, 0xffff0000, v28
	v_lshlrev_b32_e32 v42, 16, v29
	v_and_b32_e32 v43, 0xffff0000, v29
	v_lshlrev_b32_e32 v44, 16, v30
	v_and_b32_e32 v45, 0xffff0000, v30
	v_lshlrev_b32_e32 v46, 16, v31
	v_and_b32_e32 v47, 0xffff0000, v31
	v_pk_fma_f32 v[40:41], v[202:203], v[204:205], v[40:41] op_sel_hi:[0,1,1] neg_lo:[0,0,1] neg_hi:[0,0,1]
	v_pk_fma_f32 v[42:43], v[202:203], v[206:207], v[42:43] op_sel_hi:[0,1,1] neg_lo:[0,0,1] neg_hi:[0,0,1]
	v_pk_fma_f32 v[44:45], v[202:203], v[208:209], v[44:45] op_sel_hi:[0,1,1] neg_lo:[0,0,1] neg_hi:[0,0,1]
	v_pk_fma_f32 v[46:47], v[202:203], v[210:211], v[46:47] op_sel_hi:[0,1,1] neg_lo:[0,0,1] neg_hi:[0,0,1]
	v_cvt_pk_bf16_f32 v222, v40, v41
	v_cvt_pk_bf16_f32 v223, v42, v43
	v_cvt_pk_bf16_f32 v224, v44, v45
	v_cvt_pk_bf16_f32 v225, v46, v47
	global_store_dwordx4 v15, v[222:225], s[24:25]
	s_barrier
	s_branch .LBB0_678

; #define LAS __attribute__((address_space(3)))
; template <int HALFW>
; __device__ __forceinline__ void pool_item(const bf16* P, bf16* DP, LAS float* tmp, int tid, int b, int r, int g) {
;     ...
;         *(LAS f32x4*)(tmp + c * 256 + ch0) = (f32x4){acc[0] * rinv, acc[1] * rinv, acc[2] * rinv, acc[3] * rinv};
;         *(LAS f32x4*)(tmp + c * 256 + ch0 + 4) = (f32x4){acc[4] * rinv, acc[5] * rinv, acc[6] * rinv, acc[7] * rinv}; }
;     __syncthreads();
; #pragma unroll 1
;     for (int q = 0; q < 4; ++q) { const int p = tid + 512 * q, c = p >> 5, ch0 = (p & 31) * 8;
;         const int clo = c - HALFW < 0 ? 0 : c - HALFW, chi = c + HALFW > 64 ? 64 : c + HALFW; const float cinv = 1.f / (float)(chi - clo);
;         const size_t o = ((size_t)(b * 2048 + r * 64 + c)) * 1024 + g * 256 + ch0;
;         const v4u x = *(const v4u*)(P + o);
;         f32x4 a0 = (f32x4){0.f, 0.f, 0.f, 0.f}, a1 = a0;
; #pragma unroll
;         for (int u = 0; u < 2 * HALFW; ++u) { const int cc = (clo + u < chi) ? clo + u : clo; const float m = (clo + u < chi) ? 1.f : 0.f;
;             a0 += *(const LAS f32x4*)(tmp + cc * 256 + ch0) * m; a1 += *(const LAS f32x4*)(tmp + cc * 256 + ch0 + 4) * m; }
.Lpool_h8_q3:
	v_pk_mul_f32 v[52:53], v[52:53], v[48:49] op_sel_hi:[1,0]
	v_pk_mul_f32 v[54:55], v[54:55], v[48:49] op_sel_hi:[1,0]
	v_pk_mul_f32 v[56:57], v[56:57], v[48:49] op_sel_hi:[1,0]
	v_pk_mul_f32 v[58:59], v[58:59], v[48:49] op_sel_hi:[1,0]
	ds_write_b128 v49, v[52:55] offset:49152
	ds_write_b128 v49, v[56:59] offset:49168
	v_add_u32_e32 v51, 0, v50
	v_add_u32_e32 v60, 8, v51
	v_min_u32_e32 v60, 64, v60
	v_sub_u32_e64 v61, v51, 8 clamp
	v_sub_u32_e32 v60, v60, v61
	v_cvt_f32_u32_e32 v212, v60
	v_div_scale_f32 v213, s[30:31], v212, v212, 1.0
	v_div_scale_f32 v215, vcc, 1.0, v212, 1.0
	v_rcp_f32_e32 v214, v213
	s_nop 1
	v_fma_f32 v216, -v213, v214, 1.0
	v_fmac_f32_e32 v214, v216, v214
	v_mul_f32_e32 v216, v215, v214
	v_fma_f32 v217, -v213, v216, v215
	v_fmac_f32_e32 v216, v217, v214
	v_fma_f32 v213, -v213, v216, v215
	s_nop 1
	v_div_fmas_f32 v213, v213, v214, v216
	v_div_fixup_f32 v196, v213, v212, 1.0
	v_add_u32_e32 v51, 16, v50
	v_add_u32_e32 v60, 8, v51
	v_min_u32_e32 v60, 64, v60
	v_sub_u32_e64 v61, v51, 8 clamp
	v_sub_u32_e32 v60, v60, v61
	v_cvt_f32_u32_e32 v212, v60
	v_div_scale_f32 v213, s[30:31], v212, v212, 1.0
	v_div_scale_f32 v215, vcc, 1.0, v212, 1.0
	v_rcp_f32_e32 v214, v213
	s_nop 1
	v_fma_f32 v216, -v213, v214, 1.0
	v_fmac_f32_e32 v214, v216, v214
	v_mul_f32_e32 v216, v215, v214
	v_fma_f32 v217, -v213, v216, v215
	v_fmac_f32_e32 v216, v217, v214
	v_fma_f32 v213, -v213, v216, v215
	s_nop 1
	v_div_fmas_f32 v213, v213, v214, v216
	v_div_fixup_f32 v198, v213, v212, 1.0
	v_add_u32_e32 v51, 32, v50
	v_add_u32_e32 v60, 8, v51
	v_min_u32_e32 v60, 64, v60
	v_sub_u32_e64 v61, v51, 8 clamp
	v_sub_u32_e32 v60, v60, v61
	v_cvt_f32_u32_e32 v212, v60
	v_div_scale_f32 v213, s[30:31], v212, v212, 1.0
	v_div_scale_f32 v215, vcc, 1.0, v212, 1.0
	v_rcp_f32_e32 v214, v213
	s_nop 1
	v_fma_f32 v216, -v213, v214, 1.0
	v_fmac_f32_e32 v214, v216, v214
	v_mul_f32_e32 v216, v215, v214
	v_fma_f32 v217, -v213, v216, v215
	v_fmac_f32_e32 v216, v217, v214
	v_fma_f32 v213, -v213, v216, v215
	s_nop 1
	v_div_fmas_f32 v213, v213, v214, v216
	v_div_fixup_f32 v200, v213, v212, 1.0
	v_add_u32_e32 v51, 48, v50
	v_add_u32_e32 v60, 8, v51
	v_min_u32_e32 v60, 64, v60
	v_sub_u32_e64 v61, v51, 8 clamp
	v_sub_u32_e32 v60, v60, v61
	v_cvt_f32_u32_e32 v212, v60
	v_div_scale_f32 v213, s[30:31], v212, v212, 1.0
	v_div_scale_f32 v215, vcc, 1.0, v212, 1.0
	v_rcp_f32_e32 v214, v213
	s_nop 1
	v_fma_f32 v216, -v213, v214, 1.0
	v_fmac_f32_e32 v214, v216, v214
	v_mul_f32_e32 v216, v215, v214
	v_fma_f32 v217, -v213, v216, v215
	v_fmac_f32_e32 v216, v217, v214
	v_fma_f32 v213, -v213, v216, v215
	s_nop 1
	v_div_fmas_f32 v213, v213, v214, v216
	v_div_fixup_f32 v202, v213, v212, 1.0
	s_waitcnt lgkmcnt(0)
	s_barrier
	v_add_u32_e32 v51, -8, v50
	v_add_u32_e32 v60, 0, v51
	v_min_u32_e32 v60, 64, v60
	v_lshl_add_u32 v60, v60, 10, v3
	ds_read_b128 v[204:207], v60
	ds_read_b128 v[208:211], v60 offset:16
	v_add_u32_e32 v60, 1, v51
	v_min_u32_e32 v60, 64, v60
	v_lshl_add_u32 v60, v60, 10, v3
	ds_read_b128 v[76:79], v60
	ds_read_b128 v[80:83], v60 offset:16
	v_add_u32_e32 v60, 2, v51
	v_min_u32_e32 v60, 64, v60
	v_lshl_add_u32 v60, v60, 10, v3
	ds_read_b128 v[84:87], v60
	ds_read_b128 v[88:91], v60 offset:16
	v_add_u32_e32 v60, 3, v51
	v_min_u32_e32 v60, 64, v60
	v_lshl_add_u32 v60, v60, 10, v3
	ds_read_b128 v[92:95], v60
	ds_read_b128 v[96:99], v60 offset:16
	v_add_u32_e32 v60, 4, v51
	v_min_u32_e32 v60, 64, v60
	v_lshl_add_u32 v60, v60, 10, v3
	ds_read_b128 v[100:103], v60
	ds_read_b128 v[104:107], v60 offset:16
	v_add_u32_e32 v60, 5, v51
	v_min_u32_e32 v60, 64, v60
	v_lshl_add_u32 v60, v60, 10, v3
	ds_read_b128 v[108:111], v60
	ds_read_b128 v[112:115], v60 offset:16
	s_waitcnt lgkmcnt(8)
	v_pk_add_f32 v[204:205], v[204:205], v[76:77]
	v_pk_add_f32 v[206:207], v[206:207], v[78:79]
	v_pk_add_f32 v[208:209], v[208:209], v[80:81]
	v_pk_add_f32 v[210:211], v[210:211], v[82:83]
	v_add_u32_e32 v60, 6, v51
	v_min_u32_e32 v60, 64, v60
	v_lshl_add_u32 v60, v60, 10, v3
	ds_read_b128 v[68:71], v60
	ds_read_b128 v[72:75], v60 offset:16
	v_add_u32_e32 v60, 7, v51
	v_min_u32_e32 v60, 64, v60
	v_lshl_add_u32 v60, v60, 10, v3
	ds_read_b128 v[76:79], v60
	ds_read_b128 v[80:83], v60 offset:16
	s_waitcnt lgkmcnt(8)
	v_pk_add_f32 v[204:205], v[204:205], v[84:85]
	v_pk_add_f32 v[206:207], v[206:207], v[86:87]
	v_pk_add_f32 v[208:209], v[208:209], v[88:89]
	v_pk_add_f32 v[210:211], v[210:211], v[90:91]
	v_pk_add_f32 v[204:205], v[204:205], v[92:93]
	v_pk_add_f32 v[206:207], v[206:207], v[94:95]
	v_pk_add_f32 v[208:209], v[208:209], v[96:97]
	v_pk_add_f32 v[210:211], v[210:211], v[98:99]
	v_add_u32_e32 v60, 8, v51
	v_min_u32_e32 v60, 64, v60
	v_lshl_add_u32 v60, v60, 10, v3
	ds_read_b128 v[84:87], v60
	ds_read_b128 v[88:91], v60 offset:16
	v_add_u32_e32 v60, 9, v51
	v_min_u32_e32 v60, 64, v60
	v_lshl_add_u32 v60, v60, 10, v3
	ds_read_b128 v[92:95], v60
	ds_read_b128 v[96:99], v60 offset:16
	s_waitcnt lgkmcnt(8)
	v_pk_add_f32 v[204:205], v[204:205], v[100:101]
	v_pk_add_f32 v[206:207], v[206:207], v[102:103]
	v_pk_add_f32 v[208:209], v[208:209], v[104:105]
	v_pk_add_f32 v[210:211], v[210:211], v[106:107]
	v_pk_add_f32 v[204:205], v[204:205], v[108:109]
	v_pk_add_f32 v[206:207], v[206:207], v[110:111]
	v_pk_add_f32 v[208:209], v[208:209], v[112:113]
	v_pk_add_f32 v[210:211], v[210:211], v[114:115]
	v_add_u32_e32 v60, 10, v51
	v_min_u32_e32 v60, 64, v60
	v_lshl_add_u32 v60, v60, 10, v3
	ds_read_b128 v[100:103], v60
	ds_read_b128 v[104:107], v60 offset:16
	v_add_u32_e32 v60, 11, v51
	v_min_u32_e32 v60, 64, v60
	v_lshl_add_u32 v60, v60, 10, v3
	ds_read_b128 v[108:111], v60
	ds_read_b128 v[112:115], v60 offset:16
	s_waitcnt lgkmcnt(8)
; #define LAS __attribute__((address_space(3)))
; __device__ __forceinline__ unsigned pk2(float lo, float hi) { return f2bf(lo) | (f2bf(hi) << 16); }
; template <int HALFW>
; __device__ __forceinline__ void pool_item(const bf16* P, bf16* DP, LAS float* tmp, int tid, int b, int r, int g) {
;     const int rlo = r - HALFW < 0 ? 0 : r - HALFW, rhi = r + HALFW > 32 ? 32 : r + HALFW;
;     const float rinv = 1.f / (float)(rhi - rlo);
; #pragma unroll 1
;     for (int q = 0; q < 4; ++q) { const int p = tid + 512 * q, c = p >> 5, ch0 = (p & 31) * 8; float acc[8]; v4u x[2 * HALFW];
; #pragma unroll
;         for (int u = 0; u < 2 * HALFW; ++u) { const int rr = (rlo + u < rhi) ? rlo + u : rlo; x[u] = *(const v4u*)(P + ((size_t)(b * 2048 + rr * 64 + c)) * 1024 + g * 256 + ch0); }
;     ...
;     for (int q = 0; q < 4; ++q) { const int p = tid + 512 * q, c = p >> 5, ch0 = (p & 31) * 8;
;         const int clo = c - HALFW < 0 ? 0 : c - HALFW, chi = c + HALFW > 64 ? 64 : c + HALFW; const float cinv = 1.f / (float)(chi - clo);
;         const size_t o = ((size_t)(b * 2048 + r * 64 + c)) * 1024 + g * 256 + ch0;
;         const v4u x = *(const v4u*)(P + o);
;         f32x4 a0 = (f32x4){0.f, 0.f, 0.f, 0.f}, a1 = a0;
; #pragma unroll
;         for (int u = 0; u < 2 * HALFW; ++u) { const int cc = (clo + u < chi) ? clo + u : clo; const float m = (clo + u < chi) ? 1.f : 0.f;
;             a0 += *(const LAS f32x4*)(tmp + cc * 256 + ch0) * m; a1 += *(const LAS f32x4*)(tmp + cc * 256 + ch0 + 4) * m; }
;         v4u d; d.x = pk2(a0[0] * cinv - bflo(x.x), a0[1] * cinv - bfhi(x.x)); d.y = pk2(a0[2] * cinv - bflo(x.y), a0[3] * cinv - bfhi(x.y));
;         d.z = pk2(a1[0] * cinv - bflo(x.z), a1[1] * cinv - bfhi(x.z)); d.w = pk2(a1[2] * cinv - bflo(x.w), a1[3] * cinv - bfhi(x.w));
;         *(v4u*)(DP + o) = d; }
	v_pk_add_f32 v[204:205], v[204:205], v[68:69]
	v_pk_add_f32 v[206:207], v[206:207], v[70:71]
	v_pk_add_f32 v[208:209], v[208:209], v[72:73]
	v_pk_add_f32 v[210:211], v[210:211], v[74:75]
	v_pk_add_f32 v[204:205], v[204:205], v[76:77]
	v_pk_add_f32 v[206:207], v[206:207], v[78:79]
	v_pk_add_f32 v[208:209], v[208:209], v[80:81]
	v_pk_add_f32 v[210:211], v[210:211], v[82:83]
	v_add_u32_e32 v60, 12, v51
	v_min_u32_e32 v60, 64, v60
	v_lshl_add_u32 v60, v60, 10, v3
	ds_read_b128 v[68:71], v60
	ds_read_b128 v[72:75], v60 offset:16
	v_add_u32_e32 v60, 13, v51
	v_min_u32_e32 v60, 64, v60
	v_lshl_add_u32 v60, v60, 10, v3
	ds_read_b128 v[76:79], v60
	ds_read_b128 v[80:83], v60 offset:16
	s_waitcnt lgkmcnt(8)
	v_pk_add_f32 v[204:205], v[204:205], v[84:85]
	v_pk_add_f32 v[206:207], v[206:207], v[86:87]
	v_pk_add_f32 v[208:209], v[208:209], v[88:89]
	v_pk_add_f32 v[210:211], v[210:211], v[90:91]
	v_pk_add_f32 v[204:205], v[204:205], v[92:93]
	v_pk_add_f32 v[206:207], v[206:207], v[94:95]
	v_pk_add_f32 v[208:209], v[208:209], v[96:97]
	v_pk_add_f32 v[210:211], v[210:211], v[98:99]
	v_add_u32_e32 v60, 14, v51
	v_min_u32_e32 v60, 64, v60
	v_lshl_add_u32 v60, v60, 10, v3
	ds_read_b128 v[84:87], v60
	ds_read_b128 v[88:91], v60 offset:16
	v_add_u32_e32 v60, 15, v51
	v_min_u32_e32 v60, 64, v60
	v_lshl_add_u32 v60, v60, 10, v3
	ds_read_b128 v[92:95], v60
	ds_read_b128 v[96:99], v60 offset:16
	s_waitcnt lgkmcnt(8)
	v_pk_add_f32 v[204:205], v[204:205], v[100:101]
	v_pk_add_f32 v[206:207], v[206:207], v[102:103]
	v_pk_add_f32 v[208:209], v[208:209], v[104:105]
	v_pk_add_f32 v[210:211], v[210:211], v[106:107]
	v_pk_add_f32 v[204:205], v[204:205], v[108:109]
	v_pk_add_f32 v[206:207], v[206:207], v[110:111]
	v_pk_add_f32 v[208:209], v[208:209], v[112:113]
	v_pk_add_f32 v[210:211], v[210:211], v[114:115]
	s_waitcnt lgkmcnt(4)
	v_pk_add_f32 v[204:205], v[204:205], v[68:69]
	v_pk_add_f32 v[206:207], v[206:207], v[70:71]
	v_pk_add_f32 v[208:209], v[208:209], v[72:73]
	v_pk_add_f32 v[210:211], v[210:211], v[74:75]
	v_pk_add_f32 v[204:205], v[204:205], v[76:77]
	v_pk_add_f32 v[206:207], v[206:207], v[78:79]
	v_pk_add_f32 v[208:209], v[208:209], v[80:81]
	v_pk_add_f32 v[210:211], v[210:211], v[82:83]
	s_waitcnt lgkmcnt(0)
	v_pk_add_f32 v[204:205], v[204:205], v[84:85]
	v_pk_add_f32 v[206:207], v[206:207], v[86:87]
	v_pk_add_f32 v[208:209], v[208:209], v[88:89]
	v_pk_add_f32 v[210:211], v[210:211], v[90:91]
	v_pk_add_f32 v[204:205], v[204:205], v[92:93]
	v_pk_add_f32 v[206:207], v[206:207], v[94:95]
	v_pk_add_f32 v[208:209], v[208:209], v[96:97]
	v_pk_add_f32 v[210:211], v[210:211], v[98:99]
	s_waitcnt vmcnt(0)
	s_sub_i32 s39, s37, 4
	s_max_i32 s39, s39, 0
	s_add_i32 s40, s37, 4
	s_min_i32 s40, s40, 32
	s_sub_i32 s41, s40, s39
	s_add_i32 s41, s41, -1
	s_lshl_b32 s39, s39, 6
	s_add_i32 s39, s29, s39
	s_lshl_b32 s39, s39, 11
	s_add_u32 s50, s44, s39
	s_addc_u32 s51, s45, 0
	s_add_u32 s50, s50, 1024
	s_addc_u32 s51, s51, 0
	v_lshrrev_b32_e32 v240, 8, v66
	v_bfe_u32 v241, v66, 2, 6
	v_and_b32_e32 v242, 3, v66
	v_lshlrev_b32_e32 v241, 11, v241
	v_lshl_or_b32 v241, v242, 7, v241
	v_min_u32_e32 v242, s41, v240
	v_lshl_add_u32 v243, v242, 17, v241
	global_load_dword v244, v243, s[50:51]
	v_add_u32_e32 v242, 2, v240
	v_min_u32_e32 v242, s41, v242
	v_lshl_add_u32 v243, v242, 17, v241
	global_load_dword v244, v243, s[50:51]
	v_add_u32_e32 v242, 4, v240
	v_min_u32_e32 v242, s41, v242
	v_lshl_add_u32 v243, v242, 17, v241
	global_load_dword v244, v243, s[50:51]
	v_add_u32_e32 v242, 6, v240
	v_min_u32_e32 v242, s41, v242
	v_lshl_add_u32 v243, v242, 17, v241
	global_load_dword v244, v243, s[50:51]
	v_lshlrev_b32_e32 v40, 16, v16
	v_and_b32_e32 v41, 0xffff0000, v16
	v_lshlrev_b32_e32 v42, 16, v17
	v_and_b32_e32 v43, 0xffff0000, v17
	v_lshlrev_b32_e32 v44, 16, v18
	v_and_b32_e32 v45, 0xffff0000, v18
	v_lshlrev_b32_e32 v46, 16, v19
	v_and_b32_e32 v47, 0xffff0000, v19
	v_pk_fma_f32 v[40:41], v[196:197], v[204:205], v[40:41] op_sel_hi:[0,1,1] neg_lo:[0,0,1] neg_hi:[0,0,1]
	v_pk_fma_f32 v[42:43], v[196:197], v[206:207], v[42:43] op_sel_hi:[0,1,1] neg_lo:[0,0,1] neg_hi:[0,0,1]
	v_pk_fma_f32 v[44:45], v[196:197], v[208:209], v[44:45] op_sel_hi:[0,1,1] neg_lo:[0,0,1] neg_hi:[0,0,1]
	v_pk_fma_f32 v[46:47], v[196:197], v[210:211], v[46:47] op_sel_hi:[0,1,1] neg_lo:[0,0,1] neg_hi:[0,0,1]
	v_cvt_pk_bf16_f32 v218, v40, v41
	v_cvt_pk_bf16_f32 v219, v42, v43
	v_cvt_pk_bf16_f32 v220, v44, v45
	v_cvt_pk_bf16_f32 v221, v46, v47
	global_store_dwordx4 v12, v[218:221], s[24:25]
	v_add_u32_e32 v51, 8, v50
	v_add_u32_e32 v60, 0, v51
	v_min_u32_e32 v60, 64, v60
	v_lshl_add_u32 v60, v60, 10, v3
	ds_read_b128 v[204:207], v60
	ds_read_b128 v[208:211], v60 offset:16
	v_add_u32_e32 v60, 1, v51
	v_min_u32_e32 v60, 64, v60
	v_lshl_add_u32 v60, v60, 10, v3
	ds_read_b128 v[76:79], v60
	ds_read_b128 v[80:83], v60 offset:16
	v_add_u32_e32 v60, 2, v51
	v_min_u32_e32 v60, 64, v60
	v_lshl_add_u32 v60, v60, 10, v3
	ds_read_b128 v[84:87], v60
	ds_read_b128 v[88:91], v60 offset:16
	v_add_u32_e32 v60, 3, v51
	v_min_u32_e32 v60, 64, v60
	v_lshl_add_u32 v60, v60, 10, v3
	ds_read_b128 v[92:95], v60
	ds_read_b128 v[96:99], v60 offset:16
	v_add_u32_e32 v60, 4, v51
	v_min_u32_e32 v60, 64, v60
	v_lshl_add_u32 v60, v60, 10, v3
	ds_read_b128 v[100:103], v60
	ds_read_b128 v[104:107], v60 offset:16
	v_add_u32_e32 v60, 5, v51
	v_min_u32_e32 v60, 64, v60
	v_lshl_add_u32 v60, v60, 10, v3
	ds_read_b128 v[108:111], v60
	ds_read_b128 v[112:115], v60 offset:16
	s_waitcnt lgkmcnt(8)
; #define LAS __attribute__((address_space(3)))
; __device__ __forceinline__ unsigned pk2(float lo, float hi) { return f2bf(lo) | (f2bf(hi) << 16); }
; template <int HALFW>
; __device__ __forceinline__ void pool_item(const bf16* P, bf16* DP, LAS float* tmp, int tid, int b, int r, int g) {
;     ...
;     for (int q = 0; q < 4; ++q) { const int p = tid + 512 * q, c = p >> 5, ch0 = (p & 31) * 8;
;         const int clo = c - HALFW < 0 ? 0 : c - HALFW, chi = c + HALFW > 64 ? 64 : c + HALFW; const float cinv = 1.f / (float)(chi - clo);
;         const size_t o = ((size_t)(b * 2048 + r * 64 + c)) * 1024 + g * 256 + ch0;
;         const v4u x = *(const v4u*)(P + o);
;         f32x4 a0 = (f32x4){0.f, 0.f, 0.f, 0.f}, a1 = a0;
; #pragma unroll
;         for (int u = 0; u < 2 * HALFW; ++u) { const int cc = (clo + u < chi) ? clo + u : clo; const float m = (clo + u < chi) ? 1.f : 0.f;
;             a0 += *(const LAS f32x4*)(tmp + cc * 256 + ch0) * m; a1 += *(const LAS f32x4*)(tmp + cc * 256 + ch0 + 4) * m; }
;         v4u d; d.x = pk2(a0[0] * cinv - bflo(x.x), a0[1] * cinv - bfhi(x.x)); d.y = pk2(a0[2] * cinv - bflo(x.y), a0[3] * cinv - bfhi(x.y));
;         d.z = pk2(a1[0] * cinv - bflo(x.z), a1[1] * cinv - bfhi(x.z)); d.w = pk2(a1[2] * cinv - bflo(x.w), a1[3] * cinv - bfhi(x.w));
;         *(v4u*)(DP + o) = d; }
;     __syncthreads();
	v_pk_add_f32 v[204:205], v[204:205], v[76:77]
	v_pk_add_f32 v[206:207], v[206:207], v[78:79]
	v_pk_add_f32 v[208:209], v[208:209], v[80:81]
	v_pk_add_f32 v[210:211], v[210:211], v[82:83]
	v_add_u32_e32 v60, 6, v51
	v_min_u32_e32 v60, 64, v60
	v_lshl_add_u32 v60, v60, 10, v3
	ds_read_b128 v[68:71], v60
	ds_read_b128 v[72:75], v60 offset:16
	v_add_u32_e32 v60, 7, v51
	v_min_u32_e32 v60, 64, v60
	v_lshl_add_u32 v60, v60, 10, v3
	ds_read_b128 v[76:79], v60
	ds_read_b128 v[80:83], v60 offset:16
	s_waitcnt lgkmcnt(8)
	v_pk_add_f32 v[204:205], v[204:205], v[84:85]
	v_pk_add_f32 v[206:207], v[206:207], v[86:87]
	v_pk_add_f32 v[208:209], v[208:209], v[88:89]
	v_pk_add_f32 v[210:211], v[210:211], v[90:91]
	v_pk_add_f32 v[204:205], v[204:205], v[92:93]
	v_pk_add_f32 v[206:207], v[206:207], v[94:95]
	v_pk_add_f32 v[208:209], v[208:209], v[96:97]
	v_pk_add_f32 v[210:211], v[210:211], v[98:99]
	v_add_u32_e32 v60, 8, v51
	v_min_u32_e32 v60, 64, v60
	v_lshl_add_u32 v60, v60, 10, v3
	ds_read_b128 v[84:87], v60
	ds_read_b128 v[88:91], v60 offset:16
	v_add_u32_e32 v60, 9, v51
	v_min_u32_e32 v60, 64, v60
	v_lshl_add_u32 v60, v60, 10, v3
	ds_read_b128 v[92:95], v60
	ds_read_b128 v[96:99], v60 offset:16
	s_waitcnt lgkmcnt(8)
	v_pk_add_f32 v[204:205], v[204:205], v[100:101]
	v_pk_add_f32 v[206:207], v[206:207], v[102:103]
	v_pk_add_f32 v[208:209], v[208:209], v[104:105]
	v_pk_add_f32 v[210:211], v[210:211], v[106:107]
	v_pk_add_f32 v[204:205], v[204:205], v[108:109]
	v_pk_add_f32 v[206:207], v[206:207], v[110:111]
	v_pk_add_f32 v[208:209], v[208:209], v[112:113]
	v_pk_add_f32 v[210:211], v[210:211], v[114:115]
	v_add_u32_e32 v60, 10, v51
	v_min_u32_e32 v60, 64, v60
	v_lshl_add_u32 v60, v60, 10, v3
	ds_read_b128 v[100:103], v60
	ds_read_b128 v[104:107], v60 offset:16
	v_add_u32_e32 v60, 11, v51
	v_min_u32_e32 v60, 64, v60
	v_lshl_add_u32 v60, v60, 10, v3
	ds_read_b128 v[108:111], v60
	ds_read_b128 v[112:115], v60 offset:16
	s_waitcnt lgkmcnt(8)
	v_pk_add_f32 v[204:205], v[204:205], v[68:69]
	v_pk_add_f32 v[206:207], v[206:207], v[70:71]
	v_pk_add_f32 v[208:209], v[208:209], v[72:73]
	v_pk_add_f32 v[210:211], v[210:211], v[74:75]
	v_pk_add_f32 v[204:205], v[204:205], v[76:77]
	v_pk_add_f32 v[206:207], v[206:207], v[78:79]
	v_pk_add_f32 v[208:209], v[208:209], v[80:81]
	v_pk_add_f32 v[210:211], v[210:211], v[82:83]
	v_add_u32_e32 v60, 12, v51
	v_min_u32_e32 v60, 64, v60
	v_lshl_add_u32 v60, v60, 10, v3
	ds_read_b128 v[68:71], v60
	ds_read_b128 v[72:75], v60 offset:16
	v_add_u32_e32 v60, 13, v51
	v_min_u32_e32 v60, 64, v60
	v_lshl_add_u32 v60, v60, 10, v3
	ds_read_b128 v[76:79], v60
	ds_read_b128 v[80:83], v60 offset:16
	s_waitcnt lgkmcnt(8)
	v_pk_add_f32 v[204:205], v[204:205], v[84:85]
	v_pk_add_f32 v[206:207], v[206:207], v[86:87]
	v_pk_add_f32 v[208:209], v[208:209], v[88:89]
	v_pk_add_f32 v[210:211], v[210:211], v[90:91]
	v_pk_add_f32 v[204:205], v[204:205], v[92:93]
	v_pk_add_f32 v[206:207], v[206:207], v[94:95]
	v_pk_add_f32 v[208:209], v[208:209], v[96:97]
	v_pk_add_f32 v[210:211], v[210:211], v[98:99]
	v_add_u32_e32 v60, 14, v51
	v_min_u32_e32 v60, 64, v60
	v_lshl_add_u32 v60, v60, 10, v3
	ds_read_b128 v[84:87], v60
	ds_read_b128 v[88:91], v60 offset:16
	v_add_u32_e32 v60, 15, v51
	v_min_u32_e32 v60, 64, v60
	v_lshl_add_u32 v60, v60, 10, v3
	ds_read_b128 v[92:95], v60
	ds_read_b128 v[96:99], v60 offset:16
	s_waitcnt lgkmcnt(8)
	v_pk_add_f32 v[204:205], v[204:205], v[100:101]
	v_pk_add_f32 v[206:207], v[206:207], v[102:103]
	v_pk_add_f32 v[208:209], v[208:209], v[104:105]
	v_pk_add_f32 v[210:211], v[210:211], v[106:107]
	v_pk_add_f32 v[204:205], v[204:205], v[108:109]
	v_pk_add_f32 v[206:207], v[206:207], v[110:111]
	v_pk_add_f32 v[208:209], v[208:209], v[112:113]
	v_pk_add_f32 v[210:211], v[210:211], v[114:115]
	s_waitcnt lgkmcnt(4)
	v_pk_add_f32 v[204:205], v[204:205], v[68:69]
	v_pk_add_f32 v[206:207], v[206:207], v[70:71]
	v_pk_add_f32 v[208:209], v[208:209], v[72:73]
	v_pk_add_f32 v[210:211], v[210:211], v[74:75]
	v_pk_add_f32 v[204:205], v[204:205], v[76:77]
	v_pk_add_f32 v[206:207], v[206:207], v[78:79]
	v_pk_add_f32 v[208:209], v[208:209], v[80:81]
	v_pk_add_f32 v[210:211], v[210:211], v[82:83]
	s_waitcnt lgkmcnt(0)
	v_pk_add_f32 v[204:205], v[204:205], v[84:85]
	v_pk_add_f32 v[206:207], v[206:207], v[86:87]
	v_pk_add_f32 v[208:209], v[208:209], v[88:89]
	v_pk_add_f32 v[210:211], v[210:211], v[90:91]
	v_pk_add_f32 v[204:205], v[204:205], v[92:93]
	v_pk_add_f32 v[206:207], v[206:207], v[94:95]
	v_pk_add_f32 v[208:209], v[208:209], v[96:97]
	v_pk_add_f32 v[210:211], v[210:211], v[98:99]
	v_lshlrev_b32_e32 v40, 16, v20
	v_and_b32_e32 v41, 0xffff0000, v20
	v_lshlrev_b32_e32 v42, 16, v21
	v_and_b32_e32 v43, 0xffff0000, v21
	v_lshlrev_b32_e32 v44, 16, v22
	v_and_b32_e32 v45, 0xffff0000, v22
	v_lshlrev_b32_e32 v46, 16, v23
	v_and_b32_e32 v47, 0xffff0000, v23
	v_pk_fma_f32 v[40:41], v[198:199], v[204:205], v[40:41] op_sel_hi:[0,1,1] neg_lo:[0,0,1] neg_hi:[0,0,1]
	v_pk_fma_f32 v[42:43], v[198:199], v[206:207], v[42:43] op_sel_hi:[0,1,1] neg_lo:[0,0,1] neg_hi:[0,0,1]
	v_pk_fma_f32 v[44:45], v[198:199], v[208:209], v[44:45] op_sel_hi:[0,1,1] neg_lo:[0,0,1] neg_hi:[0,0,1]
	v_pk_fma_f32 v[46:47], v[198:199], v[210:211], v[46:47] op_sel_hi:[0,1,1] neg_lo:[0,0,1] neg_hi:[0,0,1]
	v_cvt_pk_bf16_f32 v222, v40, v41
	v_cvt_pk_bf16_f32 v223, v42, v43
	v_cvt_pk_bf16_f32 v224, v44, v45
	v_cvt_pk_bf16_f32 v225, v46, v47
	global_store_dwordx4 v13, v[222:225], s[24:25]
	v_add_u32_e32 v51, 24, v50
	v_add_u32_e32 v60, 0, v51
	v_min_u32_e32 v60, 64, v60
	v_lshl_add_u32 v60, v60, 10, v3
	ds_read_b128 v[204:207], v60
	ds_read_b128 v[208:211], v60 offset:16
	v_add_u32_e32 v60, 1, v51
	v_min_u32_e32 v60, 64, v60
	v_lshl_add_u32 v60, v60, 10, v3
	ds_read_b128 v[76:79], v60
	ds_read_b128 v[80:83], v60 offset:16
	v_add_u32_e32 v60, 2, v51
	v_min_u32_e32 v60, 64, v60
	v_lshl_add_u32 v60, v60, 10, v3
	ds_read_b128 v[84:87], v60
	ds_read_b128 v[88:91], v60 offset:16
	v_add_u32_e32 v60, 3, v51
	v_min_u32_e32 v60, 64, v60
	v_lshl_add_u32 v60, v60, 10, v3
	ds_read_b128 v[92:95], v60
	ds_read_b128 v[96:99], v60 offset:16
	v_add_u32_e32 v60, 4, v51
	v_min_u32_e32 v60, 64, v60
	v_lshl_add_u32 v60, v60, 10, v3
	ds_read_b128 v[100:103], v60
	ds_read_b128 v[104:107], v60 offset:16
	v_add_u32_e32 v60, 5, v51
	v_min_u32_e32 v60, 64, v60
	v_lshl_add_u32 v60, v60, 10, v3
	ds_read_b128 v[108:111], v60
	ds_read_b128 v[112:115], v60 offset:16
	s_waitcnt lgkmcnt(8)
; #define LAS __attribute__((address_space(3)))
; __device__ __forceinline__ unsigned pk2(float lo, float hi) { return f2bf(lo) | (f2bf(hi) << 16); }
; template <int HALFW>
; __device__ __forceinline__ void pool_item(const bf16* P, bf16* DP, LAS float* tmp, int tid, int b, int r, int g) {
;     ...
;     for (int q = 0; q < 4; ++q) { const int p = tid + 512 * q, c = p >> 5, ch0 = (p & 31) * 8;
;         const int clo = c - HALFW < 0 ? 0 : c - HALFW, chi = c + HALFW > 64 ? 64 : c + HALFW; const float cinv = 1.f / (float)(chi - clo);
;         const size_t o = ((size_t)(b * 2048 + r * 64 + c)) * 1024 + g * 256 + ch0;
;         const v4u x = *(const v4u*)(P + o);
;         f32x4 a0 = (f32x4){0.f, 0.f, 0.f, 0.f}, a1 = a0;
; #pragma unroll
;         for (int u = 0; u < 2 * HALFW; ++u) { const int cc = (clo + u < chi) ? clo + u : clo; const float m = (clo + u < chi) ? 1.f : 0.f;
;             a0 += *(const LAS f32x4*)(tmp + cc * 256 + ch0) * m; a1 += *(const LAS f32x4*)(tmp + cc * 256 + ch0 + 4) * m; }
;         v4u d; d.x = pk2(a0[0] * cinv - bflo(x.x), a0[1] * cinv - bfhi(x.x)); d.y = pk2(a0[2] * cinv - bflo(x.y), a0[3] * cinv - bfhi(x.y));
;         d.z = pk2(a1[0] * cinv - bflo(x.z), a1[1] * cinv - bfhi(x.z)); d.w = pk2(a1[2] * cinv - bflo(x.w), a1[3] * cinv - bfhi(x.w));
;         *(v4u*)(DP + o) = d; }
	v_pk_add_f32 v[204:205], v[204:205], v[76:77]
	v_pk_add_f32 v[206:207], v[206:207], v[78:79]
	v_pk_add_f32 v[208:209], v[208:209], v[80:81]
	v_pk_add_f32 v[210:211], v[210:211], v[82:83]
	v_add_u32_e32 v60, 6, v51
	v_min_u32_e32 v60, 64, v60
	v_lshl_add_u32 v60, v60, 10, v3
	ds_read_b128 v[68:71], v60
	ds_read_b128 v[72:75], v60 offset:16
	v_add_u32_e32 v60, 7, v51
	v_min_u32_e32 v60, 64, v60
	v_lshl_add_u32 v60, v60, 10, v3
	ds_read_b128 v[76:79], v60
	ds_read_b128 v[80:83], v60 offset:16
	s_waitcnt lgkmcnt(8)
	v_pk_add_f32 v[204:205], v[204:205], v[84:85]
	v_pk_add_f32 v[206:207], v[206:207], v[86:87]
	v_pk_add_f32 v[208:209], v[208:209], v[88:89]
	v_pk_add_f32 v[210:211], v[210:211], v[90:91]
	v_pk_add_f32 v[204:205], v[204:205], v[92:93]
	v_pk_add_f32 v[206:207], v[206:207], v[94:95]
	v_pk_add_f32 v[208:209], v[208:209], v[96:97]
	v_pk_add_f32 v[210:211], v[210:211], v[98:99]
	v_add_u32_e32 v60, 8, v51
	v_min_u32_e32 v60, 64, v60
	v_lshl_add_u32 v60, v60, 10, v3
	ds_read_b128 v[84:87], v60
	ds_read_b128 v[88:91], v60 offset:16
	v_add_u32_e32 v60, 9, v51
	v_min_u32_e32 v60, 64, v60
	v_lshl_add_u32 v60, v60, 10, v3
	ds_read_b128 v[92:95], v60
	ds_read_b128 v[96:99], v60 offset:16
	s_waitcnt lgkmcnt(8)
	v_pk_add_f32 v[204:205], v[204:205], v[100:101]
	v_pk_add_f32 v[206:207], v[206:207], v[102:103]
	v_pk_add_f32 v[208:209], v[208:209], v[104:105]
	v_pk_add_f32 v[210:211], v[210:211], v[106:107]
	v_pk_add_f32 v[204:205], v[204:205], v[108:109]
	v_pk_add_f32 v[206:207], v[206:207], v[110:111]
	v_pk_add_f32 v[208:209], v[208:209], v[112:113]
	v_pk_add_f32 v[210:211], v[210:211], v[114:115]
	v_add_u32_e32 v60, 10, v51
	v_min_u32_e32 v60, 64, v60
	v_lshl_add_u32 v60, v60, 10, v3
	ds_read_b128 v[100:103], v60
	ds_read_b128 v[104:107], v60 offset:16
	v_add_u32_e32 v60, 11, v51
	v_min_u32_e32 v60, 64, v60
	v_lshl_add_u32 v60, v60, 10, v3
	ds_read_b128 v[108:111], v60
	ds_read_b128 v[112:115], v60 offset:16
	s_waitcnt lgkmcnt(8)
	v_pk_add_f32 v[204:205], v[204:205], v[68:69]
	v_pk_add_f32 v[206:207], v[206:207], v[70:71]
	v_pk_add_f32 v[208:209], v[208:209], v[72:73]
	v_pk_add_f32 v[210:211], v[210:211], v[74:75]
	v_pk_add_f32 v[204:205], v[204:205], v[76:77]
	v_pk_add_f32 v[206:207], v[206:207], v[78:79]
	v_pk_add_f32 v[208:209], v[208:209], v[80:81]
	v_pk_add_f32 v[210:211], v[210:211], v[82:83]
	v_add_u32_e32 v60, 12, v51
	v_min_u32_e32 v60, 64, v60
	v_lshl_add_u32 v60, v60, 10, v3
	ds_read_b128 v[68:71], v60
	ds_read_b128 v[72:75], v60 offset:16
	v_add_u32_e32 v60, 13, v51
	v_min_u32_e32 v60, 64, v60
	v_lshl_add_u32 v60, v60, 10, v3
	ds_read_b128 v[76:79], v60
	ds_read_b128 v[80:83], v60 offset:16
	s_waitcnt lgkmcnt(8)
	v_pk_add_f32 v[204:205], v[204:205], v[84:85]
	v_pk_add_f32 v[206:207], v[206:207], v[86:87]
	v_pk_add_f32 v[208:209], v[208:209], v[88:89]
	v_pk_add_f32 v[210:211], v[210:211], v[90:91]
	v_pk_add_f32 v[204:205], v[204:205], v[92:93]
	v_pk_add_f32 v[206:207], v[206:207], v[94:95]
	v_pk_add_f32 v[208:209], v[208:209], v[96:97]
	v_pk_add_f32 v[210:211], v[210:211], v[98:99]
	v_add_u32_e32 v60, 14, v51
	v_min_u32_e32 v60, 64, v60
	v_lshl_add_u32 v60, v60, 10, v3
	ds_read_b128 v[84:87], v60
	ds_read_b128 v[88:91], v60 offset:16
	v_add_u32_e32 v60, 15, v51
	v_min_u32_e32 v60, 64, v60
	v_lshl_add_u32 v60, v60, 10, v3
	ds_read_b128 v[92:95], v60
	ds_read_b128 v[96:99], v60 offset:16
	s_waitcnt lgkmcnt(8)
	v_pk_add_f32 v[204:205], v[204:205], v[100:101]
	v_pk_add_f32 v[206:207], v[206:207], v[102:103]
	v_pk_add_f32 v[208:209], v[208:209], v[104:105]
	v_pk_add_f32 v[210:211], v[210:211], v[106:107]
	v_pk_add_f32 v[204:205], v[204:205], v[108:109]
	v_pk_add_f32 v[206:207], v[206:207], v[110:111]
	v_pk_add_f32 v[208:209], v[208:209], v[112:113]
	v_pk_add_f32 v[210:211], v[210:211], v[114:115]
	s_waitcnt lgkmcnt(4)
	v_pk_add_f32 v[204:205], v[204:205], v[68:69]
	v_pk_add_f32 v[206:207], v[206:207], v[70:71]
	v_pk_add_f32 v[208:209], v[208:209], v[72:73]
	v_pk_add_f32 v[210:211], v[210:211], v[74:75]
	v_pk_add_f32 v[204:205], v[204:205], v[76:77]
	v_pk_add_f32 v[206:207], v[206:207], v[78:79]
	v_pk_add_f32 v[208:209], v[208:209], v[80:81]
	v_pk_add_f32 v[210:211], v[210:211], v[82:83]
	s_waitcnt lgkmcnt(0)
	v_pk_add_f32 v[204:205], v[204:205], v[84:85]
	v_pk_add_f32 v[206:207], v[206:207], v[86:87]
	v_pk_add_f32 v[208:209], v[208:209], v[88:89]
	v_pk_add_f32 v[210:211], v[210:211], v[90:91]
	v_pk_add_f32 v[204:205], v[204:205], v[92:93]
	v_pk_add_f32 v[206:207], v[206:207], v[94:95]
	v_pk_add_f32 v[208:209], v[208:209], v[96:97]
	v_pk_add_f32 v[210:211], v[210:211], v[98:99]
	v_lshlrev_b32_e32 v40, 16, v24
	v_and_b32_e32 v41, 0xffff0000, v24
	v_lshlrev_b32_e32 v42, 16, v25
	v_and_b32_e32 v43, 0xffff0000, v25
	v_lshlrev_b32_e32 v44, 16, v26
	v_and_b32_e32 v45, 0xffff0000, v26
	v_lshlrev_b32_e32 v46, 16, v27
	v_and_b32_e32 v47, 0xffff0000, v27
	v_pk_fma_f32 v[40:41], v[200:201], v[204:205], v[40:41] op_sel_hi:[0,1,1] neg_lo:[0,0,1] neg_hi:[0,0,1]
	v_pk_fma_f32 v[42:43], v[200:201], v[206:207], v[42:43] op_sel_hi:[0,1,1] neg_lo:[0,0,1] neg_hi:[0,0,1]
	v_pk_fma_f32 v[44:45], v[200:201], v[208:209], v[44:45] op_sel_hi:[0,1,1] neg_lo:[0,0,1] neg_hi:[0,0,1]
	v_pk_fma_f32 v[46:47], v[200:201], v[210:211], v[46:47] op_sel_hi:[0,1,1] neg_lo:[0,0,1] neg_hi:[0,0,1]
	v_cvt_pk_bf16_f32 v218, v40, v41
	v_cvt_pk_bf16_f32 v219, v42, v43
	v_cvt_pk_bf16_f32 v220, v44, v45
	v_cvt_pk_bf16_f32 v221, v46, v47
	global_store_dwordx4 v14, v[218:221], s[24:25]
	v_add_u32_e32 v51, 40, v50
	v_add_u32_e32 v60, 0, v51
	v_min_u32_e32 v60, 64, v60
	v_lshl_add_u32 v60, v60, 10, v3
	ds_read_b128 v[204:207], v60
	ds_read_b128 v[208:211], v60 offset:16
	v_add_u32_e32 v60, 1, v51
	v_min_u32_e32 v60, 64, v60
	v_lshl_add_u32 v60, v60, 10, v3
	ds_read_b128 v[76:79], v60
	ds_read_b128 v[80:83], v60 offset:16
	v_add_u32_e32 v60, 2, v51
	v_min_u32_e32 v60, 64, v60
	v_lshl_add_u32 v60, v60, 10, v3
	ds_read_b128 v[84:87], v60
	ds_read_b128 v[88:91], v60 offset:16
	v_add_u32_e32 v60, 3, v51
	v_min_u32_e32 v60, 64, v60
	v_lshl_add_u32 v60, v60, 10, v3
	ds_read_b128 v[92:95], v60
	ds_read_b128 v[96:99], v60 offset:16
	v_add_u32_e32 v60, 4, v51
	v_min_u32_e32 v60, 64, v60
	v_lshl_add_u32 v60, v60, 10, v3
	ds_read_b128 v[100:103], v60
	ds_read_b128 v[104:107], v60 offset:16
	v_add_u32_e32 v60, 5, v51
	v_min_u32_e32 v60, 64, v60
	v_lshl_add_u32 v60, v60, 10, v3
	ds_read_b128 v[108:111], v60
	ds_read_b128 v[112:115], v60 offset:16
	s_waitcnt lgkmcnt(8)
; #define LAS __attribute__((address_space(3)))
; __device__ __forceinline__ unsigned pk2(float lo, float hi) { return f2bf(lo) | (f2bf(hi) << 16); }
; template <int HALFW>
; __device__ __forceinline__ void pool_item(const bf16* P, bf16* DP, LAS float* tmp, int tid, int b, int r, int g) {
;     ...
;     for (int q = 0; q < 4; ++q) { const int p = tid + 512 * q, c = p >> 5, ch0 = (p & 31) * 8;
;         const int clo = c - HALFW < 0 ? 0 : c - HALFW, chi = c + HALFW > 64 ? 64 : c + HALFW; const float cinv = 1.f / (float)(chi - clo);
;         const size_t o = ((size_t)(b * 2048 + r * 64 + c)) * 1024 + g * 256 + ch0;
;         const v4u x = *(const v4u*)(P + o);
;         f32x4 a0 = (f32x4){0.f, 0.f, 0.f, 0.f}, a1 = a0;
; #pragma unroll
;         for (int u = 0; u < 2 * HALFW; ++u) { const int cc = (clo + u < chi) ? clo + u : clo; const float m = (clo + u < chi) ? 1.f : 0.f;
;             a0 += *(const LAS f32x4*)(tmp + cc * 256 + ch0) * m; a1 += *(const LAS f32x4*)(tmp + cc * 256 + ch0 + 4) * m; }
;         v4u d; d.x = pk2(a0[0] * cinv - bflo(x.x), a0[1] * cinv - bfhi(x.x)); d.y = pk2(a0[2] * cinv - bflo(x.y), a0[3] * cinv - bfhi(x.y));
;         d.z = pk2(a1[0] * cinv - bflo(x.z), a1[1] * cinv - bfhi(x.z)); d.w = pk2(a1[2] * cinv - bflo(x.w), a1[3] * cinv - bfhi(x.w));
;         *(v4u*)(DP + o) = d; }
;     __syncthreads();
	v_pk_add_f32 v[204:205], v[204:205], v[76:77]
	v_pk_add_f32 v[206:207], v[206:207], v[78:79]
	v_pk_add_f32 v[208:209], v[208:209], v[80:81]
	v_pk_add_f32 v[210:211], v[210:211], v[82:83]
	v_add_u32_e32 v60, 6, v51
	v_min_u32_e32 v60, 64, v60
	v_lshl_add_u32 v60, v60, 10, v3
	ds_read_b128 v[68:71], v60
	ds_read_b128 v[72:75], v60 offset:16
	v_add_u32_e32 v60, 7, v51
	v_min_u32_e32 v60, 64, v60
	v_lshl_add_u32 v60, v60, 10, v3
	ds_read_b128 v[76:79], v60
	ds_read_b128 v[80:83], v60 offset:16
	s_waitcnt lgkmcnt(8)
	v_pk_add_f32 v[204:205], v[204:205], v[84:85]
	v_pk_add_f32 v[206:207], v[206:207], v[86:87]
	v_pk_add_f32 v[208:209], v[208:209], v[88:89]
	v_pk_add_f32 v[210:211], v[210:211], v[90:91]
	v_pk_add_f32 v[204:205], v[204:205], v[92:93]
	v_pk_add_f32 v[206:207], v[206:207], v[94:95]
	v_pk_add_f32 v[208:209], v[208:209], v[96:97]
	v_pk_add_f32 v[210:211], v[210:211], v[98:99]
	v_add_u32_e32 v60, 8, v51
	v_min_u32_e32 v60, 64, v60
	v_lshl_add_u32 v60, v60, 10, v3
	ds_read_b128 v[84:87], v60
	ds_read_b128 v[88:91], v60 offset:16
	v_add_u32_e32 v60, 9, v51
	v_min_u32_e32 v60, 64, v60
	v_lshl_add_u32 v60, v60, 10, v3
	ds_read_b128 v[92:95], v60
	ds_read_b128 v[96:99], v60 offset:16
	s_waitcnt lgkmcnt(8)
	v_pk_add_f32 v[204:205], v[204:205], v[100:101]
	v_pk_add_f32 v[206:207], v[206:207], v[102:103]
	v_pk_add_f32 v[208:209], v[208:209], v[104:105]
	v_pk_add_f32 v[210:211], v[210:211], v[106:107]
	v_pk_add_f32 v[204:205], v[204:205], v[108:109]
	v_pk_add_f32 v[206:207], v[206:207], v[110:111]
	v_pk_add_f32 v[208:209], v[208:209], v[112:113]
	v_pk_add_f32 v[210:211], v[210:211], v[114:115]
	v_add_u32_e32 v60, 10, v51
	v_min_u32_e32 v60, 64, v60
	v_lshl_add_u32 v60, v60, 10, v3
	ds_read_b128 v[100:103], v60
	ds_read_b128 v[104:107], v60 offset:16
	v_add_u32_e32 v60, 11, v51
	v_min_u32_e32 v60, 64, v60
	v_lshl_add_u32 v60, v60, 10, v3
	ds_read_b128 v[108:111], v60
	ds_read_b128 v[112:115], v60 offset:16
	s_waitcnt lgkmcnt(8)
	v_pk_add_f32 v[204:205], v[204:205], v[68:69]
	v_pk_add_f32 v[206:207], v[206:207], v[70:71]
	v_pk_add_f32 v[208:209], v[208:209], v[72:73]
	v_pk_add_f32 v[210:211], v[210:211], v[74:75]
	v_pk_add_f32 v[204:205], v[204:205], v[76:77]
	v_pk_add_f32 v[206:207], v[206:207], v[78:79]
	v_pk_add_f32 v[208:209], v[208:209], v[80:81]
	v_pk_add_f32 v[210:211], v[210:211], v[82:83]
	v_add_u32_e32 v60, 12, v51
	v_min_u32_e32 v60, 64, v60
	v_lshl_add_u32 v60, v60, 10, v3
	ds_read_b128 v[68:71], v60
	ds_read_b128 v[72:75], v60 offset:16
	v_add_u32_e32 v60, 13, v51
	v_min_u32_e32 v60, 64, v60
	v_lshl_add_u32 v60, v60, 10, v3
	ds_read_b128 v[76:79], v60
	ds_read_b128 v[80:83], v60 offset:16
	s_waitcnt lgkmcnt(8)
	v_pk_add_f32 v[204:205], v[204:205], v[84:85]
	v_pk_add_f32 v[206:207], v[206:207], v[86:87]
	v_pk_add_f32 v[208:209], v[208:209], v[88:89]
	v_pk_add_f32 v[210:211], v[210:211], v[90:91]
	v_pk_add_f32 v[204:205], v[204:205], v[92:93]
	v_pk_add_f32 v[206:207], v[206:207], v[94:95]
	v_pk_add_f32 v[208:209], v[208:209], v[96:97]
	v_pk_add_f32 v[210:211], v[210:211], v[98:99]
	v_add_u32_e32 v60, 14, v51
	v_min_u32_e32 v60, 64, v60
	v_lshl_add_u32 v60, v60, 10, v3
	ds_read_b128 v[84:87], v60
	ds_read_b128 v[88:91], v60 offset:16
	v_add_u32_e32 v60, 15, v51
	v_min_u32_e32 v60, 64, v60
	v_lshl_add_u32 v60, v60, 10, v3
	ds_read_b128 v[92:95], v60
	ds_read_b128 v[96:99], v60 offset:16
	s_waitcnt lgkmcnt(8)
	v_pk_add_f32 v[204:205], v[204:205], v[100:101]
	v_pk_add_f32 v[206:207], v[206:207], v[102:103]
	v_pk_add_f32 v[208:209], v[208:209], v[104:105]
	v_pk_add_f32 v[210:211], v[210:211], v[106:107]
	v_pk_add_f32 v[204:205], v[204:205], v[108:109]
	v_pk_add_f32 v[206:207], v[206:207], v[110:111]
	v_pk_add_f32 v[208:209], v[208:209], v[112:113]
	v_pk_add_f32 v[210:211], v[210:211], v[114:115]
	s_waitcnt lgkmcnt(4)
	v_pk_add_f32 v[204:205], v[204:205], v[68:69]
	v_pk_add_f32 v[206:207], v[206:207], v[70:71]
	v_pk_add_f32 v[208:209], v[208:209], v[72:73]
	v_pk_add_f32 v[210:211], v[210:211], v[74:75]
	v_pk_add_f32 v[204:205], v[204:205], v[76:77]
	v_pk_add_f32 v[206:207], v[206:207], v[78:79]
	v_pk_add_f32 v[208:209], v[208:209], v[80:81]
	v_pk_add_f32 v[210:211], v[210:211], v[82:83]
	s_waitcnt lgkmcnt(0)
	v_pk_add_f32 v[204:205], v[204:205], v[84:85]
	v_pk_add_f32 v[206:207], v[206:207], v[86:87]
	v_pk_add_f32 v[208:209], v[208:209], v[88:89]
	v_pk_add_f32 v[210:211], v[210:211], v[90:91]
	v_pk_add_f32 v[204:205], v[204:205], v[92:93]
	v_pk_add_f32 v[206:207], v[206:207], v[94:95]
	v_pk_add_f32 v[208:209], v[208:209], v[96:97]
	v_pk_add_f32 v[210:211], v[210:211], v[98:99]
	v_lshlrev_b32_e32 v40, 16, v28
	v_and_b32_e32 v41, 0xffff0000, v28
	v_lshlrev_b32_e32 v42, 16, v29
	v_and_b32_e32 v43, 0xffff0000, v29
	v_lshlrev_b32_e32 v44, 16, v30
	v_and_b32_e32 v45, 0xffff0000, v30
	v_lshlrev_b32_e32 v46, 16, v31
	v_and_b32_e32 v47, 0xffff0000, v31
	v_pk_fma_f32 v[40:41], v[202:203], v[204:205], v[40:41] op_sel_hi:[0,1,1] neg_lo:[0,0,1] neg_hi:[0,0,1]
	v_pk_fma_f32 v[42:43], v[202:203], v[206:207], v[42:43] op_sel_hi:[0,1,1] neg_lo:[0,0,1] neg_hi:[0,0,1]
	v_pk_fma_f32 v[44:45], v[202:203], v[208:209], v[44:45] op_sel_hi:[0,1,1] neg_lo:[0,0,1] neg_hi:[0,0,1]
	v_pk_fma_f32 v[46:47], v[202:203], v[210:211], v[46:47] op_sel_hi:[0,1,1] neg_lo:[0,0,1] neg_hi:[0,0,1]
	v_cvt_pk_bf16_f32 v222, v40, v41
	v_cvt_pk_bf16_f32 v223, v42, v43
	v_cvt_pk_bf16_f32 v224, v44, v45
	v_cvt_pk_bf16_f32 v225, v46, v47
	global_store_dwordx4 v15, v[222:225], s[24:25]
	s_barrier
	s_branch .LBB0_678
